# speedup vs baseline: 1.0212x; 1.0157x over previous
.LBB1_1:
	s_and_b32 s0, s29, 0x10000
	v_add_u32_e32 v211, s0, v209
	v_add_u32_e32 v242, s0, v210
	ds_read_b128 v[212:215], v242 offset:0
	ds_read_b128 v[216:219], v242 offset:0x800
	ds_read_b128 v[220:223], v242 offset:0x1000
	ds_read_b128 v[224:227], v242 offset:0x1800
	ds_read_b128 v[228:231], v211 offset:0
	ds_read_b128 v[232:235], v211 offset:0x800
	ds_read_b128 v[236:239], v211 offset:0x1000
	s_waitcnt lgkmcnt(2)
	v_mfma_f32_16x16x32_bf16 v[174:177], v[212:215], v[228:231], v[174:177]
	v_mfma_f32_16x16x32_bf16 v[170:173], v[216:219], v[228:231], v[170:173]
	v_mfma_f32_16x16x32_bf16 v[166:169], v[220:223], v[228:231], v[166:169]
	v_mfma_f32_16x16x32_bf16 v[162:165], v[224:227], v[228:231], v[162:165]
	ds_read_b128 v[228:231], v211 offset:0x1800
	s_waitcnt lgkmcnt(2)
	v_mfma_f32_16x16x32_bf16 v[158:161], v[212:215], v[232:235], v[158:161]
	v_mfma_f32_16x16x32_bf16 v[154:157], v[216:219], v[232:235], v[154:157]
	v_mfma_f32_16x16x32_bf16 v[150:153], v[220:223], v[232:235], v[150:153]
	v_mfma_f32_16x16x32_bf16 v[146:149], v[224:227], v[232:235], v[146:149]
	ds_read_b128 v[232:235], v211 offset:0x2000
	s_waitcnt lgkmcnt(2)
	v_mfma_f32_16x16x32_bf16 v[142:145], v[212:215], v[236:239], v[142:145]
	v_mfma_f32_16x16x32_bf16 v[138:141], v[216:219], v[236:239], v[138:141]
	v_mfma_f32_16x16x32_bf16 v[134:137], v[220:223], v[236:239], v[134:137]
	v_mfma_f32_16x16x32_bf16 v[130:133], v[224:227], v[236:239], v[130:133]
	ds_read_b128 v[236:239], v211 offset:0x2800
	s_waitcnt lgkmcnt(2)
	v_mfma_f32_16x16x32_bf16 v[126:129], v[212:215], v[228:231], v[126:129]
	v_mfma_f32_16x16x32_bf16 v[122:125], v[216:219], v[228:231], v[122:125]
	v_mfma_f32_16x16x32_bf16 v[118:121], v[220:223], v[228:231], v[118:121]
	v_mfma_f32_16x16x32_bf16 v[114:117], v[224:227], v[228:231], v[114:117]
	ds_read_b128 v[228:231], v211 offset:0x3000
	s_waitcnt lgkmcnt(2)
	v_mfma_f32_16x16x32_bf16 v[110:113], v[212:215], v[232:235], v[110:113]
	v_mfma_f32_16x16x32_bf16 v[106:109], v[216:219], v[232:235], v[106:109]
	v_mfma_f32_16x16x32_bf16 v[102:105], v[220:223], v[232:235], v[102:105]
	v_mfma_f32_16x16x32_bf16 v[98:101], v[224:227], v[232:235], v[98:101]
	ds_read_b128 v[232:235], v211 offset:0x3800
	s_waitcnt lgkmcnt(2)
	v_mfma_f32_16x16x32_bf16 v[94:97], v[212:215], v[236:239], v[94:97]
	v_mfma_f32_16x16x32_bf16 v[90:93], v[216:219], v[236:239], v[90:93]
	v_mfma_f32_16x16x32_bf16 v[86:89], v[220:223], v[236:239], v[86:89]
	v_mfma_f32_16x16x32_bf16 v[82:85], v[224:227], v[236:239], v[82:85]
	s_waitcnt lgkmcnt(1)
	v_mfma_f32_16x16x32_bf16 v[78:81], v[212:215], v[228:231], v[78:81]
	v_mfma_f32_16x16x32_bf16 v[74:77], v[216:219], v[228:231], v[74:77]
	v_mfma_f32_16x16x32_bf16 v[70:73], v[220:223], v[228:231], v[70:73]
	v_mfma_f32_16x16x32_bf16 v[66:69], v[224:227], v[228:231], v[66:69]
	s_waitcnt lgkmcnt(0)
	v_mfma_f32_16x16x32_bf16 v[62:65], v[212:215], v[232:235], v[62:65]
	v_mfma_f32_16x16x32_bf16 v[58:61], v[216:219], v[232:235], v[58:61]
	v_mfma_f32_16x16x32_bf16 v[54:57], v[220:223], v[232:235], v[54:57]
	v_mfma_f32_16x16x32_bf16 v[50:53], v[224:227], v[232:235], v[50:53]
	s_xor_b32 s0, s0, 0x10000
	s_and_b32 s1, s22, 0x3c0
	s_add_i32 s23, s0, 0
	s_lshl_b32 s0, s1, 2
	s_add_u32 s20, s25, s0
	s_waitcnt vmcnt(10)
	v_cvt_pk_bf16_f32 v46, v46, v47
	v_cvt_pk_bf16_f32 v47, v48, v49
	v_cvt_pk_bf16_f32 v48, v42, v43
	v_cvt_pk_bf16_f32 v49, v44, v45
	s_waitcnt vmcnt(8)
	v_cvt_pk_bf16_f32 v38, v38, v39
	v_cvt_pk_bf16_f32 v39, v40, v41
	v_cvt_pk_bf16_f32 v40, v34, v35
	v_add_u32_e32 v34, s23, v208
	s_addc_u32 s21, s26, 0
	s_lshl_b32 s0, s1, 1
	v_cvt_pk_bf16_f32 v41, v36, v37
	v_lshlrev_b32_e32 v182, 2, v178
	v_add_u32_e32 v35, s23, v205
	v_add_u32_e32 v36, s23, v206
	v_add_u32_e32 v37, s23, v207
	ds_write_b128 v34, v[46:49]
	ds_write_b128 v35, v[38:41]
	s_waitcnt vmcnt(7)
	ds_write_b128 v36, v[30:33] offset:32768
	s_waitcnt vmcnt(6)
	ds_write_b128 v37, v[26:29] offset:32768
	v_lshl_add_u64 v[26:27], s[20:21], 0, v[180:181]
	v_lshl_add_u64 v[28:29], s[20:21], 0, v[184:185]
	s_add_u32 s0, s27, s0
	v_lshl_add_u64 v[26:27], v[26:27], 0, v[182:183]
	v_lshl_add_u64 v[28:29], v[28:29], 0, v[182:183]
	s_addc_u32 s1, s28, 0
	v_lshlrev_b32_e32 v240, 1, v178
	v_mov_b32_e32 v241, v183
	global_load_dwordx4 v[42:45], v[26:27], off offset:16
	global_load_dwordx4 v[46:49], v[26:27], off
	global_load_dwordx4 v[34:37], v[28:29], off offset:16
	global_load_dwordx4 v[38:41], v[28:29], off
	v_lshl_add_u64 v[26:27], s[0:1], 0, v[186:187]
	v_lshl_add_u64 v[28:29], s[0:1], 0, v[188:189]
	v_lshl_add_u64 v[26:27], v[26:27], 0, v[240:241]
	v_lshl_add_u64 v[28:29], v[28:29], 0, v[240:241]
	global_load_dwordx4 v[30:33], v[26:27], off
	s_nop 0
	global_load_dwordx4 v[26:29], v[28:29], off
	ds_read_b128 v[212:215], v242 offset:0x400
	ds_read_b128 v[216:219], v242 offset:0xc00
	ds_read_b128 v[220:223], v242 offset:0x1400
	ds_read_b128 v[224:227], v242 offset:0x1c00
	ds_read_b128 v[228:231], v211 offset:0x400
	ds_read_b128 v[232:235], v211 offset:0xc00
	ds_read_b128 v[236:239], v211 offset:0x1400
	s_waitcnt lgkmcnt(2)
	v_mfma_f32_16x16x32_bf16 v[174:177], v[212:215], v[228:231], v[174:177]
	v_mfma_f32_16x16x32_bf16 v[170:173], v[216:219], v[228:231], v[170:173]
	v_mfma_f32_16x16x32_bf16 v[166:169], v[220:223], v[228:231], v[166:169]
	v_mfma_f32_16x16x32_bf16 v[162:165], v[224:227], v[228:231], v[162:165]
	ds_read_b128 v[228:231], v211 offset:0x1c00
	s_waitcnt lgkmcnt(2)
	v_mfma_f32_16x16x32_bf16 v[158:161], v[212:215], v[232:235], v[158:161]
	v_mfma_f32_16x16x32_bf16 v[154:157], v[216:219], v[232:235], v[154:157]
	v_mfma_f32_16x16x32_bf16 v[150:153], v[220:223], v[232:235], v[150:153]
	v_mfma_f32_16x16x32_bf16 v[146:149], v[224:227], v[232:235], v[146:149]
	ds_read_b128 v[232:235], v211 offset:0x2400
	s_waitcnt lgkmcnt(2)
	v_mfma_f32_16x16x32_bf16 v[142:145], v[212:215], v[236:239], v[142:145]
	v_mfma_f32_16x16x32_bf16 v[138:141], v[216:219], v[236:239], v[138:141]
	v_mfma_f32_16x16x32_bf16 v[134:137], v[220:223], v[236:239], v[134:137]
	v_mfma_f32_16x16x32_bf16 v[130:133], v[224:227], v[236:239], v[130:133]
	ds_read_b128 v[236:239], v211 offset:0x2c00
	s_waitcnt lgkmcnt(2)
	v_mfma_f32_16x16x32_bf16 v[126:129], v[212:215], v[228:231], v[126:129]
	v_mfma_f32_16x16x32_bf16 v[122:125], v[216:219], v[228:231], v[122:125]
	v_mfma_f32_16x16x32_bf16 v[118:121], v[220:223], v[228:231], v[118:121]
	v_mfma_f32_16x16x32_bf16 v[114:117], v[224:227], v[228:231], v[114:117]
	ds_read_b128 v[228:231], v211 offset:0x3400
	s_waitcnt lgkmcnt(2)
	v_mfma_f32_16x16x32_bf16 v[110:113], v[212:215], v[232:235], v[110:113]
	v_mfma_f32_16x16x32_bf16 v[106:109], v[216:219], v[232:235], v[106:109]
	v_mfma_f32_16x16x32_bf16 v[102:105], v[220:223], v[232:235], v[102:105]
	v_mfma_f32_16x16x32_bf16 v[98:101], v[224:227], v[232:235], v[98:101]
	ds_read_b128 v[232:235], v211 offset:0x3c00
	s_waitcnt lgkmcnt(2)
	v_mfma_f32_16x16x32_bf16 v[94:97], v[212:215], v[236:239], v[94:97]
	v_mfma_f32_16x16x32_bf16 v[90:93], v[216:219], v[236:239], v[90:93]
	v_mfma_f32_16x16x32_bf16 v[86:89], v[220:223], v[236:239], v[86:89]
	v_mfma_f32_16x16x32_bf16 v[82:85], v[224:227], v[236:239], v[82:85]
	s_waitcnt lgkmcnt(1)
	v_mfma_f32_16x16x32_bf16 v[78:81], v[212:215], v[228:231], v[78:81]
	v_mfma_f32_16x16x32_bf16 v[74:77], v[216:219], v[228:231], v[74:77]
	v_mfma_f32_16x16x32_bf16 v[70:73], v[220:223], v[228:231], v[70:73]
	v_mfma_f32_16x16x32_bf16 v[66:69], v[224:227], v[228:231], v[66:69]
	s_waitcnt lgkmcnt(0)
	v_mfma_f32_16x16x32_bf16 v[62:65], v[212:215], v[232:235], v[62:65]
	v_mfma_f32_16x16x32_bf16 v[58:61], v[216:219], v[232:235], v[58:61]
	v_mfma_f32_16x16x32_bf16 v[54:57], v[220:223], v[232:235], v[54:57]
	v_mfma_f32_16x16x32_bf16 v[50:53], v[224:227], v[232:235], v[50:53]
	s_waitcnt vmcnt(10)
	v_cvt_pk_bf16_f32 v22, v22, v23
	v_cvt_pk_bf16_f32 v23, v24, v25
	v_cvt_pk_bf16_f32 v24, v6, v7
	v_cvt_pk_bf16_f32 v25, v8, v9
	v_add_u32_e32 v6, s23, v204
	s_waitcnt vmcnt(9)
	v_cvt_pk_bf16_f32 v8, v2, v3
	v_add_u32_e32 v2, s23, v201
	ds_write_b128 v6, v[22:25]
	s_waitcnt vmcnt(8)
	v_cvt_pk_bf16_f32 v6, v10, v11
	v_cvt_pk_bf16_f32 v7, v12, v13
	v_cvt_pk_bf16_f32 v9, v4, v5
	ds_write_b128 v2, v[6:9]
	v_add_u32_e32 v2, s23, v202
	s_waitcnt vmcnt(7)
	ds_write_b128 v2, v[18:21] offset:32768
	v_add_u32_e32 v2, s23, v203
	s_waitcnt vmcnt(6)
	ds_write_b128 v2, v[14:17] offset:32768
	v_lshl_add_u64 v[2:3], s[20:21], 0, v[190:191]
	v_lshl_add_u64 v[2:3], v[2:3], 0, v[182:183]
	global_load_dwordx4 v[6:9], v[2:3], off offset:16
	global_load_dwordx4 v[22:25], v[2:3], off
	v_lshl_add_u64 v[2:3], s[20:21], 0, v[192:193]
	v_lshl_add_u64 v[14:15], s[0:1], 0, v[194:195]
	v_lshl_add_u64 v[16:17], s[0:1], 0, v[196:197]
	v_lshl_add_u64 v[10:11], v[2:3], 0, v[182:183]
	v_lshl_add_u64 v[14:15], v[14:15], 0, v[240:241]
	v_lshl_add_u64 v[16:17], v[16:17], 0, v[240:241]
	global_load_dwordx4 v[2:5], v[10:11], off offset:16
	s_nop 0
	global_load_dwordx4 v[10:13], v[10:11], off
	s_nop 0
	global_load_dwordx4 v[18:21], v[14:15], off
	s_nop 0
	global_load_dwordx4 v[14:17], v[16:17], off
	s_waitcnt lgkmcnt(0)
	s_add_i32 s22, s22, 64
	s_add_i32 s29, s29, 0x10000
	s_cmp_lg_u32 s29, 0xe0000
	s_barrier
	s_cbranch_scc1 .LBB1_1
	s_lshl_b64 s[0:1], s[18:19], 24
	ds_read_b128 v[180:183], v210 offset:0
	ds_read_b128 v[184:187], v210 offset:0x800
	ds_read_b128 v[188:191], v210 offset:0x1000
	ds_read_b128 v[192:195], v210 offset:0x1800
	ds_read_b128 v[212:215], v209 offset:0
	ds_read_b128 v[216:219], v209 offset:0x800
	ds_read_b128 v[220:223], v209 offset:0x1000
	s_waitcnt lgkmcnt(0)
	s_add_u32 s0, s10, s0
	s_addc_u32 s18, s11, s1
	s_lshl_b32 s19, s24, 1
	s_mov_b32 s1, 0
	s_add_u32 s0, s0, s19
	s_waitcnt lgkmcnt(2)
	s_addc_u32 s20, s18, 0
	v_mfma_f32_16x16x32_bf16 v[174:177], v[180:183], v[212:215], v[174:177]
	v_mfma_f32_16x16x32_bf16 v[170:173], v[184:187], v[212:215], v[170:173]
	v_mfma_f32_16x16x32_bf16 v[166:169], v[188:191], v[212:215], v[166:169]
	v_mfma_f32_16x16x32_bf16 v[162:165], v[192:195], v[212:215], v[162:165]
	ds_read_b128 v[212:215], v209 offset:0x1800
	s_waitcnt lgkmcnt(2)
	s_nop 0
	v_mfma_f32_16x16x32_bf16 v[158:161], v[180:183], v[216:219], v[158:161]
	v_mfma_f32_16x16x32_bf16 v[154:157], v[184:187], v[216:219], v[154:157]
	v_mfma_f32_16x16x32_bf16 v[150:153], v[188:191], v[216:219], v[150:153]
	v_mfma_f32_16x16x32_bf16 v[146:149], v[192:195], v[216:219], v[146:149]
	ds_read_b128 v[216:219], v209 offset:0x2000
	s_waitcnt lgkmcnt(2)
	s_nop 0
	v_mfma_f32_16x16x32_bf16 v[142:145], v[180:183], v[220:223], v[142:145]
	v_mfma_f32_16x16x32_bf16 v[138:141], v[184:187], v[220:223], v[138:141]
	v_mfma_f32_16x16x32_bf16 v[134:137], v[188:191], v[220:223], v[134:137]
	v_mfma_f32_16x16x32_bf16 v[130:133], v[192:195], v[220:223], v[130:133]
	ds_read_b128 v[220:223], v209 offset:0x2800
	s_waitcnt lgkmcnt(2)
	s_nop 0
	v_mfma_f32_16x16x32_bf16 v[126:129], v[180:183], v[212:215], v[126:129]
	v_mfma_f32_16x16x32_bf16 v[122:125], v[184:187], v[212:215], v[122:125]
	v_mfma_f32_16x16x32_bf16 v[118:121], v[188:191], v[212:215], v[118:121]
	v_mfma_f32_16x16x32_bf16 v[114:117], v[192:195], v[212:215], v[114:117]
	ds_read_b128 v[212:215], v209 offset:0x3000
	s_waitcnt lgkmcnt(2)
	s_nop 0
	v_mfma_f32_16x16x32_bf16 v[110:113], v[180:183], v[216:219], v[110:113]
	v_mfma_f32_16x16x32_bf16 v[106:109], v[184:187], v[216:219], v[106:109]
	v_mfma_f32_16x16x32_bf16 v[102:105], v[188:191], v[216:219], v[102:105]
	v_mfma_f32_16x16x32_bf16 v[98:101], v[192:195], v[216:219], v[98:101]
	ds_read_b128 v[216:219], v209 offset:0x3800
	s_waitcnt lgkmcnt(2)
	s_nop 0
	v_mfma_f32_16x16x32_bf16 v[94:97], v[180:183], v[220:223], v[94:97]
	v_mfma_f32_16x16x32_bf16 v[90:93], v[184:187], v[220:223], v[90:93]
	v_mfma_f32_16x16x32_bf16 v[86:89], v[188:191], v[220:223], v[86:89]
	v_mfma_f32_16x16x32_bf16 v[82:85], v[192:195], v[220:223], v[82:85]
	s_waitcnt lgkmcnt(1)
	s_nop 0
	v_mfma_f32_16x16x32_bf16 v[78:81], v[180:183], v[212:215], v[78:81]
	v_mfma_f32_16x16x32_bf16 v[74:77], v[184:187], v[212:215], v[74:77]
	v_mfma_f32_16x16x32_bf16 v[70:73], v[188:191], v[212:215], v[70:73]
	v_mfma_f32_16x16x32_bf16 v[66:69], v[192:195], v[212:215], v[66:69]
	s_waitcnt lgkmcnt(0)
	s_nop 0
	v_mfma_f32_16x16x32_bf16 v[62:65], v[180:183], v[216:219], v[62:65]
	v_mfma_f32_16x16x32_bf16 v[58:61], v[184:187], v[216:219], v[58:61]
	v_mfma_f32_16x16x32_bf16 v[54:57], v[188:191], v[216:219], v[54:57]
	v_mfma_f32_16x16x32_bf16 v[50:53], v[192:195], v[216:219], v[50:53]
	s_add_i32 s18, 0, 0x10000
	s_waitcnt vmcnt(10)
	v_cvt_pk_bf16_f32 v46, v46, v47
	v_cvt_pk_bf16_f32 v47, v48, v49
	v_cvt_pk_bf16_f32 v48, v42, v43
	v_add_u32_e32 v42, s18, v208
	s_waitcnt vmcnt(8)
	v_cvt_pk_bf16_f32 v38, v38, v39
	v_cvt_pk_bf16_f32 v39, v40, v41
	v_cvt_pk_bf16_f32 v40, v34, v35
	v_add_u32_e32 v34, s18, v205
	s_add_i32 s19, 0, 0x18000
	v_cvt_pk_bf16_f32 v49, v44, v45
	ds_write_b128 v42, v[46:49]
	v_cvt_pk_bf16_f32 v41, v36, v37
	ds_write_b128 v34, v[38:41]
	v_add_u32_e32 v34, s19, v206
	s_waitcnt vmcnt(7)
	ds_write_b128 v34, v[30:33]
	v_add_u32_e32 v30, s19, v207
	s_waitcnt vmcnt(6)
	ds_write_b128 v30, v[26:29]
	ds_read_b128 v[26:29], v210 offset:0x400
	ds_read_b128 v[30:33], v210 offset:0xc00
	ds_read_b128 v[34:37], v210 offset:0x1400
	ds_read_b128 v[38:41], v210 offset:0x1c00
	ds_read_b128 v[42:45], v209 offset:0x400
	ds_read_b128 v[46:49], v209 offset:0xc00
	ds_read_b128 v[180:183], v209 offset:0x1400
	s_nop 0
	s_waitcnt lgkmcnt(2)
	s_nop 0
	v_mfma_f32_16x16x32_bf16 v[174:177], v[26:29], v[42:45], v[174:177]
	v_mfma_f32_16x16x32_bf16 v[170:173], v[30:33], v[42:45], v[170:173]
	v_mfma_f32_16x16x32_bf16 v[166:169], v[34:37], v[42:45], v[166:169]
	v_mfma_f32_16x16x32_bf16 v[42:45], v[38:41], v[42:45], v[162:165]
	ds_read_b128 v[162:165], v209 offset:0x1c00
	s_waitcnt lgkmcnt(2)
	s_nop 0
	v_mfma_f32_16x16x32_bf16 v[158:161], v[26:29], v[46:49], v[158:161]
	v_mfma_f32_16x16x32_bf16 v[154:157], v[30:33], v[46:49], v[154:157]
	v_mfma_f32_16x16x32_bf16 v[150:153], v[34:37], v[46:49], v[150:153]
	v_mfma_f32_16x16x32_bf16 v[46:49], v[38:41], v[46:49], v[146:149]
	ds_read_b128 v[146:149], v209 offset:0x2400
	s_waitcnt lgkmcnt(2)
	s_nop 0
	v_mfma_f32_16x16x32_bf16 v[142:145], v[26:29], v[180:183], v[142:145]
	v_mfma_f32_16x16x32_bf16 v[138:141], v[30:33], v[180:183], v[138:141]
	v_mfma_f32_16x16x32_bf16 v[134:137], v[34:37], v[180:183], v[134:137]
	v_mfma_f32_16x16x32_bf16 v[130:133], v[38:41], v[180:183], v[130:133]
	ds_read_b128 v[180:183], v209 offset:0x2c00
	s_waitcnt lgkmcnt(2)
	s_nop 0
	v_mfma_f32_16x16x32_bf16 v[126:129], v[26:29], v[162:165], v[126:129]
	v_mfma_f32_16x16x32_bf16 v[122:125], v[30:33], v[162:165], v[122:125]
	v_mfma_f32_16x16x32_bf16 v[118:121], v[34:37], v[162:165], v[118:121]
	v_mfma_f32_16x16x32_bf16 v[114:117], v[38:41], v[162:165], v[114:117]
	ds_read_b128 v[162:165], v209 offset:0x3400
	s_waitcnt lgkmcnt(2)
	s_nop 0
	v_mfma_f32_16x16x32_bf16 v[110:113], v[26:29], v[146:149], v[110:113]
	v_mfma_f32_16x16x32_bf16 v[106:109], v[30:33], v[146:149], v[106:109]
	v_mfma_f32_16x16x32_bf16 v[102:105], v[34:37], v[146:149], v[102:105]
	v_mfma_f32_16x16x32_bf16 v[98:101], v[38:41], v[146:149], v[98:101]
	ds_read_b128 v[146:149], v209 offset:0x3c00
	s_waitcnt lgkmcnt(2)
	s_nop 0
	v_mfma_f32_16x16x32_bf16 v[94:97], v[26:29], v[180:183], v[94:97]
	v_mfma_f32_16x16x32_bf16 v[90:93], v[30:33], v[180:183], v[90:93]
	v_mfma_f32_16x16x32_bf16 v[86:89], v[34:37], v[180:183], v[86:89]
	v_mfma_f32_16x16x32_bf16 v[82:85], v[38:41], v[180:183], v[82:85]
	s_waitcnt lgkmcnt(1)
	s_nop 0
	v_mfma_f32_16x16x32_bf16 v[78:81], v[26:29], v[162:165], v[78:81]
	v_mfma_f32_16x16x32_bf16 v[74:77], v[30:33], v[162:165], v[74:77]
	v_mfma_f32_16x16x32_bf16 v[70:73], v[34:37], v[162:165], v[70:73]
	v_mfma_f32_16x16x32_bf16 v[66:69], v[38:41], v[162:165], v[66:69]
	s_waitcnt lgkmcnt(0)
	s_nop 0
	v_mfma_f32_16x16x32_bf16 v[26:29], v[26:29], v[146:149], v[62:65]
	v_mfma_f32_16x16x32_bf16 v[30:33], v[30:33], v[146:149], v[58:61]
	v_mfma_f32_16x16x32_bf16 v[34:37], v[34:37], v[146:149], v[54:57]
	v_mfma_f32_16x16x32_bf16 v[38:41], v[38:41], v[146:149], v[50:53]
	s_waitcnt vmcnt(4)
	v_cvt_pk_bf16_f32 v22, v22, v23
	v_cvt_pk_bf16_f32 v23, v24, v25
	v_cvt_pk_bf16_f32 v24, v6, v7
	v_cvt_pk_bf16_f32 v25, v8, v9
	v_add_u32_e32 v6, s18, v204
	s_waitcnt vmcnt(3)
	v_cvt_pk_bf16_f32 v8, v2, v3
	v_add_u32_e32 v2, s18, v201
	ds_write_b128 v6, v[22:25]
	s_waitcnt vmcnt(2)
	v_cvt_pk_bf16_f32 v6, v10, v11
	v_cvt_pk_bf16_f32 v7, v12, v13
	v_cvt_pk_bf16_f32 v9, v4, v5
	ds_write_b128 v2, v[6:9]
	v_add_u32_e32 v2, s19, v202
	s_waitcnt vmcnt(1)
	ds_write_b128 v2, v[18:21]
	v_add_u32_e32 v2, s19, v203
	s_waitcnt vmcnt(0)
	ds_write_b128 v2, v[14:17]
	s_waitcnt lgkmcnt(0)
	s_barrier
	v_add_u32_e32 v178, 0x10000, v209
	v_add_u32_e32 v196, 0x10000, v210
	ds_read_b128 v[2:5], v196 offset:0
	ds_read_b128 v[6:9], v196 offset:0x800
	ds_read_b128 v[10:13], v196 offset:0x1000
	ds_read_b128 v[14:17], v196 offset:0x1800
	ds_read_b128 v[18:21], v178 offset:0
	s_and_b64 s[16:17], s[16:17], exec
	ds_read_b128 v[22:25], v178 offset:0x800
	ds_read_b128 v[50:53], v178 offset:0x1000
	s_waitcnt lgkmcnt(2)
	s_cselect_b32 s5, s5, s7
	s_cselect_b32 s4, s4, s6
	s_lshl_b32 s6, s3, 10
	v_mfma_f32_16x16x32_bf16 v[54:57], v[2:5], v[18:21], v[174:177]
	s_add_u32 s6, s4, s6
	s_addc_u32 s7, s5, 0
	s_lshl_b32 s3, s3, 9
	v_mfma_f32_16x16x32_bf16 v[58:61], v[6:9], v[18:21], v[170:173]
	s_add_u32 s4, s0, s3
	s_addc_u32 s5, s20, 0
	v_mfma_f32_16x16x32_bf16 v[62:65], v[10:13], v[18:21], v[166:169]
	v_mfma_f32_16x16x32_bf16 v[18:21], v[14:17], v[18:21], v[42:45]
	ds_read_b128 v[42:45], v178 offset:0x1800
	s_waitcnt lgkmcnt(2)
	s_nop 0
	v_mfma_f32_16x16x32_bf16 v[146:149], v[2:5], v[22:25], v[158:161]
	v_mfma_f32_16x16x32_bf16 v[154:157], v[6:9], v[22:25], v[154:157]
	v_mfma_f32_16x16x32_bf16 v[150:153], v[10:13], v[22:25], v[150:153]
	v_mfma_f32_16x16x32_bf16 v[22:25], v[14:17], v[22:25], v[46:49]
	ds_read_b128 v[46:49], v178 offset:0x2000
	s_waitcnt lgkmcnt(2)
	s_nop 0
	v_mfma_f32_16x16x32_bf16 v[142:145], v[2:5], v[50:53], v[142:145]
	v_mfma_f32_16x16x32_bf16 v[138:141], v[6:9], v[50:53], v[138:141]
	v_mfma_f32_16x16x32_bf16 v[134:137], v[10:13], v[50:53], v[134:137]
	v_mfma_f32_16x16x32_bf16 v[50:53], v[14:17], v[50:53], v[130:133]
	ds_read_b128 v[130:133], v178 offset:0x2800
	s_waitcnt lgkmcnt(2)
	s_nop 0
	v_mfma_f32_16x16x32_bf16 v[126:129], v[2:5], v[42:45], v[126:129]
	v_mfma_f32_16x16x32_bf16 v[122:125], v[6:9], v[42:45], v[122:125]
	v_mfma_f32_16x16x32_bf16 v[118:121], v[10:13], v[42:45], v[118:121]
	v_mfma_f32_16x16x32_bf16 v[42:45], v[14:17], v[42:45], v[114:117]
	ds_read_b128 v[114:117], v178 offset:0x3000
	s_waitcnt lgkmcnt(2)
	s_nop 0
	v_mfma_f32_16x16x32_bf16 v[110:113], v[2:5], v[46:49], v[110:113]
	v_mfma_f32_16x16x32_bf16 v[106:109], v[6:9], v[46:49], v[106:109]
	v_mfma_f32_16x16x32_bf16 v[102:105], v[10:13], v[46:49], v[102:105]
	v_mfma_f32_16x16x32_bf16 v[98:101], v[14:17], v[46:49], v[98:101]
	ds_read_b128 v[46:49], v178 offset:0x3800
	s_waitcnt lgkmcnt(2)
	s_nop 0
	v_mfma_f32_16x16x32_bf16 v[158:161], v[2:5], v[130:133], v[94:97]
	v_mfma_f32_16x16x32_bf16 v[162:165], v[6:9], v[130:133], v[90:93]
	v_mfma_f32_16x16x32_bf16 v[166:169], v[10:13], v[130:133], v[86:89]
	v_mfma_f32_16x16x32_bf16 v[130:133], v[14:17], v[130:133], v[82:85]
	s_waitcnt lgkmcnt(1)
	s_nop 0
	v_mfma_f32_16x16x32_bf16 v[66:69], v[14:17], v[114:117], v[66:69]
	v_mfma_f32_16x16x32_bf16 v[170:173], v[2:5], v[114:117], v[78:81]
	v_mfma_f32_16x16x32_bf16 v[174:177], v[6:9], v[114:117], v[74:77]
	v_mfma_f32_16x16x32_bf16 v[180:183], v[10:13], v[114:117], v[70:73]
	s_waitcnt lgkmcnt(0)
	s_nop 0
	v_mfma_f32_16x16x32_bf16 v[2:5], v[2:5], v[46:49], v[26:29]
	v_mfma_f32_16x16x32_bf16 v[114:117], v[6:9], v[46:49], v[30:33]
	v_mfma_f32_16x16x32_bf16 v[34:37], v[10:13], v[46:49], v[34:37]
	v_mfma_f32_16x16x32_bf16 v[184:187], v[14:17], v[46:49], v[38:41]
	ds_read_b128 v[188:191], v196 offset:0x400
	ds_read_b128 v[192:195], v196 offset:0xc00
	ds_read_b128 v[202:205], v196 offset:0x1400
	ds_read_b128 v[206:209], v196 offset:0x1c00
	ds_read_b128 v[6:9], v178 offset:0x400
	ds_read_b128 v[10:13], v178 offset:0xc00
	ds_read_b128 v[14:17], v178 offset:0x1400
	s_nop 0
	s_waitcnt lgkmcnt(2)
	s_nop 0
	v_mfma_f32_16x16x32_bf16 v[94:97], v[192:195], v[6:9], v[58:61]
	v_mfma_f32_16x16x32_bf16 v[62:65], v[202:205], v[6:9], v[62:65]
	v_mfma_f32_16x16x32_bf16 v[30:33], v[206:209], v[6:9], v[18:21]
	v_mfma_f32_16x16x32_bf16 v[210:213], v[188:191], v[6:9], v[54:57]
	ds_read_b128 v[6:9], v178 offset:0x1c00
	s_waitcnt lgkmcnt(2)
	s_nop 0
	v_mfma_f32_16x16x32_bf16 v[90:93], v[192:195], v[10:13], v[154:157]
	v_mfma_f32_16x16x32_bf16 v[58:61], v[202:205], v[10:13], v[150:153]
	v_mfma_f32_16x16x32_bf16 v[26:29], v[206:209], v[10:13], v[22:25]
	v_mfma_f32_16x16x32_bf16 v[146:149], v[188:191], v[10:13], v[146:149]
	ds_read_b128 v[10:13], v178 offset:0x2400
	s_waitcnt lgkmcnt(2)
	s_nop 0
	v_mfma_f32_16x16x32_bf16 v[86:89], v[192:195], v[14:17], v[138:141]
	v_mfma_f32_16x16x32_bf16 v[54:57], v[202:205], v[14:17], v[134:137]
	v_mfma_f32_16x16x32_bf16 v[22:25], v[206:209], v[14:17], v[50:53]
	v_mfma_f32_16x16x32_bf16 v[142:145], v[188:191], v[14:17], v[142:145]
	ds_read_b128 v[38:41], v178 offset:0x2c00
	s_waitcnt lgkmcnt(2)
	s_nop 0
	v_mfma_f32_16x16x32_bf16 v[126:129], v[188:191], v[6:9], v[126:129]
	v_mfma_f32_16x16x32_bf16 v[82:85], v[192:195], v[6:9], v[122:125]
	v_mfma_f32_16x16x32_bf16 v[50:53], v[202:205], v[6:9], v[118:121]
	v_mfma_f32_16x16x32_bf16 v[18:21], v[206:209], v[6:9], v[42:45]
	ds_read_b128 v[6:9], v178 offset:0x3400
	s_waitcnt lgkmcnt(2)
	s_nop 0
	v_mfma_f32_16x16x32_bf16 v[110:113], v[188:191], v[10:13], v[110:113]
	v_mfma_f32_16x16x32_bf16 v[78:81], v[192:195], v[10:13], v[106:109]
	v_mfma_f32_16x16x32_bf16 v[46:49], v[202:205], v[10:13], v[102:105]
	v_mfma_f32_16x16x32_bf16 v[14:17], v[206:209], v[10:13], v[98:101]
	ds_read_b128 v[98:101], v178 offset:0x3c00
	s_waitcnt lgkmcnt(2)
	s_nop 0
	v_mfma_f32_16x16x32_bf16 v[106:109], v[188:191], v[38:41], v[158:161]
	v_mfma_f32_16x16x32_bf16 v[74:77], v[192:195], v[38:41], v[162:165]
	v_mfma_f32_16x16x32_bf16 v[42:45], v[202:205], v[38:41], v[166:169]
	v_mfma_f32_16x16x32_bf16 v[10:13], v[206:209], v[38:41], v[130:133]
	s_waitcnt lgkmcnt(1)
	s_nop 0
	v_mfma_f32_16x16x32_bf16 v[118:121], v[188:191], v[6:9], v[170:173]
	v_mfma_f32_16x16x32_bf16 v[70:73], v[192:195], v[6:9], v[174:177]
	v_mfma_f32_16x16x32_bf16 v[38:41], v[202:205], v[6:9], v[180:183]
	v_mfma_f32_16x16x32_bf16 v[6:9], v[206:209], v[6:9], v[66:69]
	s_waitcnt lgkmcnt(0)
	s_nop 0
	v_mfma_f32_16x16x32_bf16 v[122:125], v[188:191], v[98:101], v[2:5]
	v_mfma_f32_16x16x32_bf16 v[66:69], v[192:195], v[98:101], v[114:117]
	v_mfma_f32_16x16x32_bf16 v[34:37], v[202:205], v[98:101], v[34:37]
	v_mfma_f32_16x16x32_bf16 v[2:5], v[206:209], v[98:101], v[184:187]
	v_lshrrev_b32_e32 v98, 2, v199
	v_and_b32_e32 v98, 12, v98
	v_lshl_or_b32 v104, v200, 6, v98
	v_lshlrev_b32_e32 v105, 2, v104
	s_waitcnt lgkmcnt(0)
	s_barrier
	global_load_dwordx4 v[114:117], v105, s[6:7]
	v_lshrrev_b32_e32 v98, 1, v199
	v_lshlrev_b32_e32 v99, 16, v198
	v_lshlrev_b32_e32 v100, 9, v179
	v_and_b32_e32 v102, 8, v98
	v_lshrrev_b32_e32 v98, 3, v104
	v_add3_u32 v103, 0, v99, v100
	v_xor_b32_e32 v130, v98, v179
	v_bitop3_b32 v131, v98, v179, 16 bitop3:0x1e
	global_load_dwordx4 v[98:101], v105, s[6:7] offset:64
	v_lshlrev_b32_e32 v130, 4, v130
	v_lshlrev_b32_e32 v131, 4, v131
	v_add3_u32 v130, v103, v130, v102
	v_add3_u32 v131, v103, v131, v102
	s_movk_i32 s0, 0x200
	s_waitcnt vmcnt(1)
	v_add_f32_e32 v132, v210, v114
	v_add_f32_e32 v133, v211, v115
	v_add_f32_e32 v134, v212, v116
	v_add_f32_e32 v135, v213, v117
	v_add_f32_e32 v140, v142, v114
	v_add_f32_e32 v141, v143, v115
	v_add_f32_e32 v142, v144, v116
	v_add_f32_e32 v143, v145, v117
	v_add_f32_e32 v110, v110, v114
	v_add_f32_e32 v111, v111, v115
	v_add_f32_e32 v106, v106, v114
	v_add_f32_e32 v107, v107, v115
	v_add_f32_e32 v136, v146, v114
	v_add_f32_e32 v137, v147, v115
	v_add_f32_e32 v138, v148, v116
	v_add_f32_e32 v139, v149, v117
	v_add_f32_e32 v126, v126, v114
	v_add_f32_e32 v127, v127, v115
	v_add_f32_e32 v128, v128, v116
	v_add_f32_e32 v129, v129, v117
	v_add_f32_e32 v112, v112, v116
	v_add_f32_e32 v113, v113, v117
	v_add_f32_e32 v108, v108, v116
	v_add_f32_e32 v109, v109, v117
	v_max_f32_e32 v132, 0, v132
	v_max_f32_e32 v133, 0, v133
	v_max_f32_e32 v134, 0, v134
	v_max_f32_e32 v135, 0, v135
	v_max_f32_e32 v140, 0, v140
	v_max_f32_e32 v141, 0, v141
	v_max_f32_e32 v142, 0, v142
	v_max_f32_e32 v143, 0, v143
	v_max_f32_e32 v144, 0, v110
	v_max_f32_e32 v145, 0, v111
	v_max_f32_e32 v148, 0, v106
	v_max_f32_e32 v149, 0, v107
	v_cvt_pk_bf16_f32 v106, v132, v133
	v_cvt_pk_bf16_f32 v107, v134, v135
	v_cvt_pk_bf16_f32 v110, v140, v141
	v_cvt_pk_bf16_f32 v111, v142, v143
	v_add_f32_e32 v118, v118, v114
	v_add_f32_e32 v119, v119, v115
	v_max_f32_e32 v136, 0, v136
	v_max_f32_e32 v137, 0, v137
	v_max_f32_e32 v138, 0, v138
	v_max_f32_e32 v139, 0, v139
	v_max_f32_e32 v126, 0, v126
	v_max_f32_e32 v127, 0, v127
	v_max_f32_e32 v128, 0, v128
	v_max_f32_e32 v129, 0, v129
	v_max_f32_e32 v146, 0, v112
	v_max_f32_e32 v147, 0, v113
	v_max_f32_e32 v150, 0, v108
	v_max_f32_e32 v151, 0, v109
	v_cvt_pk_bf16_f32 v108, v136, v137
	v_cvt_pk_bf16_f32 v109, v138, v139
	v_cvt_pk_bf16_f32 v112, v126, v127
	v_cvt_pk_bf16_f32 v113, v128, v129
	ds_write2st64_b64 v130, v[106:107], v[110:111] offset1:32
	ds_write2st64_b64 v131, v[108:109], v[112:113] offset0:16 offset1:48
	v_add_f32_e32 v106, v121, v117
	v_add_f32_e32 v120, v120, v116
	v_max_f32_e32 v152, 0, v118
	v_max_f32_e32 v153, 0, v119
	v_max_f32_e32 v107, 0, v106
	v_cvt_pk_bf16_f32 v106, v152, v153
	v_max_f32_e32 v120, 0, v120
	v_cvt_pk_bf16_f32 v118, v144, v145
	v_cvt_pk_bf16_f32 v119, v146, v147
	v_cvt_pk_bf16_f32 v107, v120, v107
	ds_write2st64_b64 v130, v[118:119], v[106:107] offset0:64 offset1:96
	v_add_f32_e32 v106, v122, v114
	v_max_f32_e32 v106, 0, v106
	v_add_f32_e32 v107, v123, v115
	v_max_f32_e32 v107, 0, v107
	v_add_f32_e32 v108, v124, v116
	v_add_f32_e32 v109, v125, v117
	v_cvt_pk_bf16_f32 v106, v106, v107
	v_cvt_pk_bf16_f32 v126, v148, v149
	v_cvt_pk_bf16_f32 v127, v150, v151
	v_max_f32_e32 v108, 0, v108
	v_max_f32_e32 v109, 0, v109
	v_cvt_pk_bf16_f32 v107, v108, v109
	ds_write2st64_b64 v131, v[126:127], v[106:107] offset0:80 offset1:112
	v_or_b32_e32 v106, 16, v104
	s_waitcnt vmcnt(0)
	v_add_f32_e32 v94, v94, v98
	v_add_f32_e32 v95, v95, v99
	v_add_f32_e32 v96, v96, v100
	v_lshrrev_b32_e32 v106, 3, v106
	v_max_f32_e32 v94, 0, v94
	v_max_f32_e32 v95, 0, v95
	v_max_f32_e32 v96, 0, v96
	v_add_f32_e32 v97, v97, v101
	v_max_f32_e32 v97, 0, v97
	v_cvt_pk_bf16_f32 v94, v94, v95
	v_cvt_pk_bf16_f32 v95, v96, v97
	v_xor_b32_e32 v96, v106, v179
	v_lshlrev_b32_e32 v96, 4, v96
	v_add3_u32 v107, v103, v96, v102
	v_add_f32_e32 v90, v90, v98
	v_add_f32_e32 v91, v91, v99
	v_add_f32_e32 v92, v92, v100
	ds_write_b64 v107, v[94:95]
	v_max_f32_e32 v90, 0, v90
	v_max_f32_e32 v91, 0, v91
	global_load_dwordx4 v[94:97], v105, s[6:7] offset:128
	v_max_f32_e32 v92, 0, v92
	v_add_f32_e32 v93, v93, v101
	v_max_f32_e32 v93, 0, v93
	v_cvt_pk_bf16_f32 v90, v90, v91
	v_cvt_pk_bf16_f32 v91, v92, v93
	v_bitop3_b32 v92, v106, v179, 16 bitop3:0x1e
	v_add_f32_e32 v66, v66, v98
	v_lshlrev_b32_e32 v92, 4, v92
	v_add_f32_e32 v86, v86, v98
	v_add_f32_e32 v87, v87, v99
	v_add_f32_e32 v82, v82, v98
	v_add_f32_e32 v83, v83, v99
	v_add_f32_e32 v78, v78, v98
	v_add_f32_e32 v79, v79, v99
	v_add_f32_e32 v74, v74, v98
	v_add_f32_e32 v75, v75, v99
	v_add_f32_e32 v70, v70, v98
	v_add_f32_e32 v71, v71, v99
	v_max_f32_e32 v66, 0, v66
	v_add_f32_e32 v67, v67, v99
	v_add3_u32 v92, v103, v92, v102
	v_max_f32_e32 v86, 0, v86
	v_max_f32_e32 v87, 0, v87
	v_add_f32_e32 v88, v88, v100
	v_add_f32_e32 v89, v89, v101
	v_max_f32_e32 v82, 0, v82
	v_max_f32_e32 v83, 0, v83
	v_add_f32_e32 v84, v84, v100
	v_add_f32_e32 v85, v85, v101
	v_max_f32_e32 v78, 0, v78
	v_max_f32_e32 v79, 0, v79
	v_add_f32_e32 v80, v80, v100
	v_add_f32_e32 v81, v81, v101
	v_max_f32_e32 v74, 0, v74
	v_max_f32_e32 v75, 0, v75
	v_add_f32_e32 v76, v76, v100
	v_add_f32_e32 v77, v77, v101
	v_max_f32_e32 v70, 0, v70
	v_max_f32_e32 v71, 0, v71
	v_add_f32_e32 v72, v72, v100
	v_add_f32_e32 v73, v73, v101
	v_max_f32_e32 v67, 0, v67
	v_add_f32_e32 v68, v68, v100
	v_add_f32_e32 v69, v69, v101
	v_cvt_pk_bf16_f32 v66, v66, v67
	ds_write_b64 v92, v[90:91] offset:8192
	v_max_f32_e32 v88, 0, v88
	v_max_f32_e32 v89, 0, v89
	v_cvt_pk_bf16_f32 v86, v86, v87
	v_cvt_pk_bf16_f32 v87, v88, v89
	ds_write_b64 v107, v[86:87] offset:16384
	v_max_f32_e32 v84, 0, v84
	v_max_f32_e32 v85, 0, v85
	v_cvt_pk_bf16_f32 v82, v82, v83
	v_cvt_pk_bf16_f32 v83, v84, v85
	ds_write_b64 v92, v[82:83] offset:24576
	v_max_f32_e32 v80, 0, v80
	v_max_f32_e32 v81, 0, v81
	v_cvt_pk_bf16_f32 v78, v78, v79
	v_cvt_pk_bf16_f32 v79, v80, v81
	ds_write_b64 v107, v[78:79] offset:32768
	v_max_f32_e32 v76, 0, v76
	v_max_f32_e32 v77, 0, v77
	v_cvt_pk_bf16_f32 v74, v74, v75
	v_cvt_pk_bf16_f32 v75, v76, v77
	ds_write_b64 v92, v[74:75] offset:40960
	v_max_f32_e32 v72, 0, v72
	v_max_f32_e32 v73, 0, v73
	v_cvt_pk_bf16_f32 v70, v70, v71
	v_cvt_pk_bf16_f32 v71, v72, v73
	ds_write_b64 v107, v[70:71] offset:49152
	v_max_f32_e32 v68, 0, v68
	v_max_f32_e32 v69, 0, v69
	v_cvt_pk_bf16_f32 v67, v68, v69
	ds_write_b64 v92, v[66:67] offset:57344
	v_or_b32_e32 v66, 32, v104
	v_lshrrev_b32_e32 v70, 3, v66
	global_load_dwordx4 v[66:69], v105, s[6:7] offset:192
	s_waitcnt vmcnt(1)
	v_add_f32_e32 v62, v62, v94
	v_add_f32_e32 v63, v63, v95
	v_add_f32_e32 v64, v64, v96
	v_add_f32_e32 v58, v58, v94
	v_add_f32_e32 v59, v59, v95
	v_add_f32_e32 v60, v60, v96
	v_max_f32_e32 v62, 0, v62
	v_max_f32_e32 v63, 0, v63
	v_max_f32_e32 v64, 0, v64
	v_add_f32_e32 v65, v65, v97
	v_max_f32_e32 v58, 0, v58
	v_max_f32_e32 v59, 0, v59
	v_max_f32_e32 v60, 0, v60
	v_add_f32_e32 v61, v61, v97
	v_max_f32_e32 v65, 0, v65
	v_cvt_pk_bf16_f32 v62, v62, v63
	v_cvt_pk_bf16_f32 v63, v64, v65
	v_xor_b32_e32 v64, v70, v179
	v_max_f32_e32 v61, 0, v61
	v_cvt_pk_bf16_f32 v58, v58, v59
	v_cvt_pk_bf16_f32 v59, v60, v61
	v_bitop3_b32 v60, v70, v179, 16 bitop3:0x1e
	v_add_f32_e32 v34, v34, v94
	v_lshlrev_b32_e32 v64, 4, v64
	v_lshlrev_b32_e32 v60, 4, v60
	v_add_f32_e32 v54, v54, v94
	v_add_f32_e32 v55, v55, v95
	v_add_f32_e32 v50, v50, v94
	v_add_f32_e32 v51, v51, v95
	v_add_f32_e32 v46, v46, v94
	v_add_f32_e32 v47, v47, v95
	v_add_f32_e32 v42, v42, v94
	v_add_f32_e32 v43, v43, v95
	v_add_f32_e32 v38, v38, v94
	v_add_f32_e32 v39, v39, v95
	v_max_f32_e32 v34, 0, v34
	v_add_f32_e32 v35, v35, v95
	v_add3_u32 v64, v103, v64, v102
	v_add3_u32 v60, v103, v60, v102
	v_max_f32_e32 v54, 0, v54
	v_max_f32_e32 v55, 0, v55
	v_add_f32_e32 v56, v56, v96
	v_add_f32_e32 v57, v57, v97
	v_max_f32_e32 v50, 0, v50
	v_max_f32_e32 v51, 0, v51
	v_add_f32_e32 v52, v52, v96
	v_add_f32_e32 v53, v53, v97
	v_max_f32_e32 v46, 0, v46
	v_max_f32_e32 v47, 0, v47
	v_add_f32_e32 v48, v48, v96
	v_add_f32_e32 v49, v49, v97
	v_max_f32_e32 v42, 0, v42
	v_max_f32_e32 v43, 0, v43
	v_add_f32_e32 v44, v44, v96
	v_add_f32_e32 v45, v45, v97
	v_max_f32_e32 v38, 0, v38
	v_max_f32_e32 v39, 0, v39
	v_add_f32_e32 v40, v40, v96
	v_add_f32_e32 v41, v41, v97
	v_max_f32_e32 v35, 0, v35
	v_add_f32_e32 v36, v36, v96
	v_add_f32_e32 v37, v37, v97
	v_cvt_pk_bf16_f32 v34, v34, v35
	ds_write_b64 v64, v[62:63]
	ds_write_b64 v60, v[58:59] offset:8192
	v_max_f32_e32 v56, 0, v56
	v_max_f32_e32 v57, 0, v57
	v_cvt_pk_bf16_f32 v54, v54, v55
	v_cvt_pk_bf16_f32 v55, v56, v57
	ds_write_b64 v64, v[54:55] offset:16384
	v_max_f32_e32 v52, 0, v52
	v_max_f32_e32 v53, 0, v53
	v_cvt_pk_bf16_f32 v50, v50, v51
	v_cvt_pk_bf16_f32 v51, v52, v53
	ds_write_b64 v60, v[50:51] offset:24576
	v_max_f32_e32 v48, 0, v48
	v_max_f32_e32 v49, 0, v49
	v_cvt_pk_bf16_f32 v46, v46, v47
	v_cvt_pk_bf16_f32 v47, v48, v49
	ds_write_b64 v64, v[46:47] offset:32768
	v_max_f32_e32 v44, 0, v44
	v_max_f32_e32 v45, 0, v45
	v_cvt_pk_bf16_f32 v42, v42, v43
	v_cvt_pk_bf16_f32 v43, v44, v45
	ds_write_b64 v60, v[42:43] offset:40960
	v_max_f32_e32 v40, 0, v40
	v_max_f32_e32 v41, 0, v41
	v_cvt_pk_bf16_f32 v38, v38, v39
	v_cvt_pk_bf16_f32 v39, v40, v41
	ds_write_b64 v64, v[38:39] offset:49152
	v_max_f32_e32 v36, 0, v36
	v_max_f32_e32 v37, 0, v37
	v_cvt_pk_bf16_f32 v35, v36, v37
	ds_write_b64 v60, v[34:35] offset:57344
	v_or_b32_e32 v34, 48, v104
	s_waitcnt vmcnt(0)
	v_add_f32_e32 v30, v30, v66
	v_add_f32_e32 v31, v31, v67
	v_add_f32_e32 v32, v32, v68
	v_add_f32_e32 v26, v26, v66
	v_add_f32_e32 v27, v27, v67
	v_add_f32_e32 v28, v28, v68
	v_lshrrev_b32_e32 v34, 3, v34
	v_max_f32_e32 v30, 0, v30
	v_max_f32_e32 v31, 0, v31
	v_max_f32_e32 v32, 0, v32
	v_add_f32_e32 v33, v33, v69
	v_max_f32_e32 v26, 0, v26
	v_max_f32_e32 v27, 0, v27
	v_max_f32_e32 v28, 0, v28
	v_add_f32_e32 v29, v29, v69
	v_max_f32_e32 v33, 0, v33
	v_cvt_pk_bf16_f32 v30, v30, v31
	v_cvt_pk_bf16_f32 v31, v32, v33
	v_xor_b32_e32 v32, v34, v179
	v_max_f32_e32 v29, 0, v29
	v_cvt_pk_bf16_f32 v26, v26, v27
	v_cvt_pk_bf16_f32 v27, v28, v29
	v_bitop3_b32 v28, v34, v179, 16 bitop3:0x1e
	v_add_f32_e32 v2, v2, v66
	v_lshlrev_b32_e32 v32, 4, v32
	v_lshlrev_b32_e32 v28, 4, v28
	v_add_f32_e32 v22, v22, v66
	v_add_f32_e32 v23, v23, v67
	v_add_f32_e32 v18, v18, v66
	v_add_f32_e32 v19, v19, v67
	v_add_f32_e32 v14, v14, v66
	v_add_f32_e32 v15, v15, v67
	v_add_f32_e32 v10, v10, v66
	v_add_f32_e32 v11, v11, v67
	v_add_f32_e32 v6, v6, v66
	v_add_f32_e32 v7, v7, v67
	v_max_f32_e32 v2, 0, v2
	v_add_f32_e32 v3, v3, v67
	v_add3_u32 v32, v103, v32, v102
	v_add3_u32 v28, v103, v28, v102
	v_max_f32_e32 v22, 0, v22
	v_max_f32_e32 v23, 0, v23
	v_add_f32_e32 v24, v24, v68
	v_add_f32_e32 v25, v25, v69
	v_max_f32_e32 v18, 0, v18
	v_max_f32_e32 v19, 0, v19
	v_add_f32_e32 v20, v20, v68
	v_add_f32_e32 v21, v21, v69
	v_max_f32_e32 v14, 0, v14
	v_max_f32_e32 v15, 0, v15
	v_add_f32_e32 v16, v16, v68
	v_add_f32_e32 v17, v17, v69
	v_max_f32_e32 v10, 0, v10
	v_max_f32_e32 v11, 0, v11
	v_add_f32_e32 v12, v12, v68
	v_add_f32_e32 v13, v13, v69
	v_max_f32_e32 v6, 0, v6
	v_max_f32_e32 v7, 0, v7
	v_add_f32_e32 v8, v8, v68
	v_add_f32_e32 v9, v9, v69
	v_max_f32_e32 v3, 0, v3
	v_add_f32_e32 v4, v4, v68
	v_add_f32_e32 v5, v5, v69
	v_cvt_pk_bf16_f32 v2, v2, v3
	ds_write_b64 v32, v[30:31]
	ds_write_b64 v28, v[26:27] offset:8192
	v_max_f32_e32 v24, 0, v24
	v_max_f32_e32 v25, 0, v25
	v_cvt_pk_bf16_f32 v22, v22, v23
	v_cvt_pk_bf16_f32 v23, v24, v25
	ds_write_b64 v32, v[22:23] offset:16384
	v_max_f32_e32 v20, 0, v20
	v_max_f32_e32 v21, 0, v21
	v_cvt_pk_bf16_f32 v18, v18, v19
	v_cvt_pk_bf16_f32 v19, v20, v21
	ds_write_b64 v28, v[18:19] offset:24576
	v_max_f32_e32 v16, 0, v16
	v_max_f32_e32 v17, 0, v17
	v_cvt_pk_bf16_f32 v14, v14, v15
	v_cvt_pk_bf16_f32 v15, v16, v17
	ds_write_b64 v32, v[14:15] offset:32768
	v_max_f32_e32 v12, 0, v12
	v_max_f32_e32 v13, 0, v13
	v_cvt_pk_bf16_f32 v10, v10, v11
	v_cvt_pk_bf16_f32 v11, v12, v13
	ds_write_b64 v28, v[10:11] offset:40960
	v_max_f32_e32 v8, 0, v8
	v_max_f32_e32 v9, 0, v9
	v_cvt_pk_bf16_f32 v6, v6, v7
	v_cvt_pk_bf16_f32 v7, v8, v9
	ds_write_b64 v32, v[6:7] offset:49152
	v_max_f32_e32 v4, 0, v4
	v_max_f32_e32 v5, 0, v5
	v_cvt_pk_bf16_f32 v3, v4, v5
	ds_write_b64 v28, v[2:3] offset:57344
	v_and_b32_e32 v2, 0x1f0, v1
	v_lshrrev_b32_e32 v1, 5, v0
	v_xor_b32_e32 v4, v1, v0
	v_mov_b32_e32 v3, 0
	v_lshlrev_b32_e32 v4, 4, v4
	v_lshl_add_u64 v[12:13], s[4:5], 0, v[2:3]
	v_lshlrev_b32_e32 v2, 9, v1
	v_and_b32_e32 v16, 0x1f0, v4
	v_add3_u32 v2, 0, v2, v16
	s_waitcnt lgkmcnt(0)
	s_barrier
	ds_read_b128 v[4:7], v2
	v_lshlrev_b32_e32 v2, 11, v1
	v_lshl_add_u64 v[14:15], v[12:13], 0, v[2:3]
	v_or_b32_e32 v2, 0x200, v0
	v_lshrrev_b32_e32 v2, 5, v2
	v_xor_b32_e32 v9, v2, v0
	v_lshlrev_b32_e32 v9, 4, v9
	v_lshlrev_b32_e32 v8, 9, v2
	v_and_b32_e32 v9, 0x1f0, v9
	v_add3_u32 v8, 0, v8, v9
	ds_read_b128 v[8:11], v8
	v_lshlrev_b32_e32 v2, 11, v2
	s_waitcnt lgkmcnt(1)
	global_store_dwordx4 v[14:15], v[4:7], off sc1
	s_nop 1
	v_lshl_add_u64 v[4:5], v[12:13], 0, v[2:3]
	s_waitcnt lgkmcnt(0)
	global_store_dwordx4 v[4:5], v[8:11], off sc1
	v_or_b32_e32 v2, 32, v1
	v_lshlrev_b32_e32 v4, 9, v2
	v_or_b32_e32 v8, 0x600, v0
	v_lshrrev_b32_e32 v17, 5, v8
	v_xor_b32_e32 v9, v17, v0
	v_lshlrev_b32_e32 v9, 4, v9
	v_add3_u32 v4, 0, v4, v16
	v_lshlrev_b32_e32 v8, 9, v17
	v_and_b32_e32 v9, 0x1f0, v9
	ds_read_b128 v[4:7], v4
	v_add3_u32 v8, 0, v8, v9
	ds_read_b128 v[8:11], v8
	v_lshlrev_b32_e32 v2, 11, v2
	v_lshl_add_u64 v[14:15], v[12:13], 0, v[2:3]
	v_lshlrev_b32_e32 v2, 11, v17
	s_waitcnt lgkmcnt(1)
	global_store_dwordx4 v[14:15], v[4:7], off sc1
	s_nop 1
	v_lshl_add_u64 v[4:5], v[12:13], 0, v[2:3]
	s_waitcnt lgkmcnt(0)
	global_store_dwordx4 v[4:5], v[8:11], off sc1
	v_or_b32_e32 v2, 64, v1
	v_lshlrev_b32_e32 v4, 9, v2
	v_or_b32_e32 v8, 0xa00, v0
	v_lshrrev_b32_e32 v17, 5, v8
	v_xor_b32_e32 v9, v17, v0
	v_lshlrev_b32_e32 v9, 4, v9
	v_add3_u32 v4, 0, v4, v16
	v_lshlrev_b32_e32 v8, 9, v17
	v_and_b32_e32 v9, 0x1f0, v9
	ds_read_b128 v[4:7], v4
	v_add3_u32 v8, 0, v8, v9
	ds_read_b128 v[8:11], v8
	v_lshlrev_b32_e32 v2, 11, v2
	v_lshl_add_u64 v[14:15], v[12:13], 0, v[2:3]
	v_lshlrev_b32_e32 v2, 11, v17
	s_waitcnt lgkmcnt(1)
	global_store_dwordx4 v[14:15], v[4:7], off sc1
	s_nop 1
	v_lshl_add_u64 v[4:5], v[12:13], 0, v[2:3]
	s_waitcnt lgkmcnt(0)
	global_store_dwordx4 v[4:5], v[8:11], off sc1
	v_or_b32_e32 v2, 0x60, v1
	v_lshlrev_b32_e32 v4, 9, v2
	v_or_b32_e32 v8, 0xe00, v0
	v_lshrrev_b32_e32 v17, 5, v8
	v_xor_b32_e32 v9, v17, v0
	v_lshlrev_b32_e32 v9, 4, v9
	v_add3_u32 v4, 0, v4, v16
	v_lshlrev_b32_e32 v8, 9, v17
	v_and_b32_e32 v9, 0x1f0, v9
	ds_read_b128 v[4:7], v4
	v_add3_u32 v8, 0, v8, v9
	ds_read_b128 v[8:11], v8
	v_lshlrev_b32_e32 v2, 11, v2
	v_lshl_add_u64 v[14:15], v[12:13], 0, v[2:3]
	v_lshlrev_b32_e32 v2, 11, v17
	s_waitcnt lgkmcnt(1)
	global_store_dwordx4 v[14:15], v[4:7], off sc1
	s_nop 1
	v_lshl_add_u64 v[4:5], v[12:13], 0, v[2:3]
	s_waitcnt lgkmcnt(0)
	global_store_dwordx4 v[4:5], v[8:11], off sc1
	v_or_b32_e32 v2, 0x80, v1
	v_lshlrev_b32_e32 v4, 9, v2
	v_or_b32_e32 v8, 0x1200, v0
	v_lshrrev_b32_e32 v17, 5, v8
	v_xor_b32_e32 v9, v17, v0
	v_lshlrev_b32_e32 v9, 4, v9
	v_add3_u32 v4, 0, v4, v16
	v_lshlrev_b32_e32 v8, 9, v17
	v_and_b32_e32 v9, 0x1f0, v9
	ds_read_b128 v[4:7], v4
	v_add3_u32 v8, 0, v8, v9
	ds_read_b128 v[8:11], v8
	v_lshlrev_b32_e32 v2, 11, v2
	v_lshl_add_u64 v[14:15], v[12:13], 0, v[2:3]
	v_lshlrev_b32_e32 v2, 11, v17
	s_waitcnt lgkmcnt(1)
	global_store_dwordx4 v[14:15], v[4:7], off sc1
	s_nop 1
	v_lshl_add_u64 v[4:5], v[12:13], 0, v[2:3]
	s_waitcnt lgkmcnt(0)
	global_store_dwordx4 v[4:5], v[8:11], off sc1
	v_or_b32_e32 v2, 0xa0, v1
	v_lshlrev_b32_e32 v4, 9, v2
	v_or_b32_e32 v8, 0x1600, v0
	v_lshrrev_b32_e32 v17, 5, v8
	v_xor_b32_e32 v9, v17, v0
	v_lshlrev_b32_e32 v9, 4, v9
	v_add3_u32 v4, 0, v4, v16
	v_lshlrev_b32_e32 v8, 9, v17
	v_and_b32_e32 v9, 0x1f0, v9
	ds_read_b128 v[4:7], v4
	v_add3_u32 v8, 0, v8, v9
	ds_read_b128 v[8:11], v8
	v_lshlrev_b32_e32 v2, 11, v2
	v_lshl_add_u64 v[14:15], v[12:13], 0, v[2:3]
	v_lshlrev_b32_e32 v2, 11, v17
	s_waitcnt lgkmcnt(1)
	global_store_dwordx4 v[14:15], v[4:7], off sc1
	s_nop 1
	v_lshl_add_u64 v[4:5], v[12:13], 0, v[2:3]
	s_waitcnt lgkmcnt(0)
	global_store_dwordx4 v[4:5], v[8:11], off sc1
	v_or_b32_e32 v2, 0xc0, v1
	v_lshlrev_b32_e32 v4, 9, v2
	v_or_b32_e32 v8, 0x1a00, v0
	v_lshrrev_b32_e32 v17, 5, v8
	v_xor_b32_e32 v9, v17, v0
	v_add3_u32 v4, 0, v4, v16
	v_lshlrev_b32_e32 v9, 4, v9
	ds_read_b128 v[4:7], v4
	v_lshlrev_b32_e32 v8, 9, v17
	v_and_b32_e32 v9, 0x1f0, v9
	v_add3_u32 v8, 0, v8, v9
	ds_read_b128 v[8:11], v8
	v_lshlrev_b32_e32 v2, 11, v2
	v_lshl_add_u64 v[14:15], v[12:13], 0, v[2:3]
	v_lshlrev_b32_e32 v2, 11, v17
	v_or_b32_e32 v1, 0xe0, v1
	s_waitcnt lgkmcnt(1)
	global_store_dwordx4 v[14:15], v[4:7], off sc1
	s_nop 1
	v_lshl_add_u64 v[4:5], v[12:13], 0, v[2:3]
	v_lshlrev_b32_e32 v2, 9, v1
	v_add3_u32 v2, 0, v2, v16
	s_waitcnt lgkmcnt(0)
	global_store_dwordx4 v[4:5], v[8:11], off sc1
	ds_read_b128 v[4:7], v2
	v_lshlrev_b32_e32 v2, 11, v1
	v_or_b32_e32 v1, 0x1e00, v0
	v_lshrrev_b32_e32 v1, 5, v1
	v_xor_b32_e32 v9, v1, v0
	v_lshlrev_b32_e32 v9, 4, v9
	v_lshlrev_b32_e32 v8, 9, v1
	v_and_b32_e32 v9, 0x1f0, v9
	v_add3_u32 v8, 0, v8, v9
	ds_read_b128 v[8:11], v8
	v_lshl_add_u64 v[14:15], v[12:13], 0, v[2:3]
	v_lshlrev_b32_e32 v2, 11, v1
	s_waitcnt lgkmcnt(1)
	global_store_dwordx4 v[14:15], v[4:7], off sc1
	s_nop 1
	v_lshl_add_u64 v[4:5], v[12:13], 0, v[2:3]
	s_waitcnt lgkmcnt(0)
	global_store_dwordx4 v[4:5], v[8:11], off sc1
	s_waitcnt lgkmcnt(0)
	s_barrier
	s_lshl_b32 s3, s2, 3
	s_and_b32 s3, s3, 56
	s_ashr_i32 s17, s2, 5
	s_add_i32 s20, s3, s17
	s_ashr_i32 s21, s20, 31
	s_bfe_u32 s16, s2, 0x20003
	s_lshl_b64 s[4:5], s[20:21], 17
	s_lshl_b64 s[6:7], s[20:21], 19
	s_add_u32 s6, s12, s6
	s_addc_u32 s7, s13, s7
	s_lshl_b32 s3, s16, 19
	s_add_u32 s3, s14, s3
	v_ashrrev_i32_e32 v2, 6, v0
	v_lshlrev_b32_e32 v1, 4, v0
	s_addc_u32 s13, s15, 0
	v_lshlrev_b32_e32 v4, 9, v2
	v_and_b32_e32 v5, 0x1f0, v1
	s_add_u32 s12, s3, 0x400000
	v_and_or_b32 v32, v4, s0, v5
	v_lshlrev_b32_e32 v4, 5, v2
	v_and_b32_e32 v5, 48, v1
	s_addc_u32 s13, s13, 0
	v_bitop3_b32 v4, v4, v5, 32 bitop3:0x6c
	s_and_b32 s15, s2, 8
	s_add_i32 s3, s20, 3
	v_bfe_u32 v31, v0, 5, 1
	v_lshrrev_b32_e32 v34, 1, v4
	v_add_u32_e32 v4, s15, v2
	s_mov_b32 s20, 0x3ffffe
	v_and_or_b32 v30, v4, s20, v31
	v_bfe_i32 v5, v30, 0, 22
	v_bfe_u32 v4, v30, 21, 1
	v_add_u32_e32 v6, v5, v4
	v_lshlrev_b32_e32 v4, 3, v6
	v_and_b32_e32 v6, 0x7fffffe, v6
	s_lshl_b32 s0, s17, 4
	v_sub_u32_e32 v5, v5, v6
	s_and_b32 s17, s0, 16
	v_lshl_or_b32 v6, v5, 5, v34
	v_add_u32_e32 v5, s17, v2
	v_and_or_b32 v35, v5, s20, v31
	v_bfe_i32 v7, v35, 0, 22
	v_bfe_u32 v8, v35, 21, 1
	v_add_u32_e32 v8, v7, v8
	v_lshlrev_b32_e32 v9, 3, v8
	v_and_b32_e32 v8, 0x7fffffe, v8
	v_add_u32_e32 v5, 8, v5
	v_sub_u32_e32 v7, v7, v8
	v_and_or_b32 v36, v5, s20, v31
	v_lshl_or_b32 v98, v7, 5, v34
	v_bfe_i32 v5, v36, 0, 22
	v_bfe_u32 v7, v36, 21, 1
	v_add_u32_e32 v7, v5, v7
	v_lshrrev_b32_e32 v33, 6, v32
	v_lshlrev_b32_e32 v8, 3, v7
	v_and_b32_e32 v7, 0x7fffffe, v7
	s_and_b32 s3, s3, 15
	v_and_or_b32 v4, v4, -16, v33
	v_sub_u32_e32 v5, v5, v7
	v_and_or_b32 v14, v9, -16, v33
	v_lshl_or_b32 v100, v5, 5, v34
	v_ashrrev_i32_e32 v5, 31, v4
	s_lshl_b32 s14, s3, 6
	s_lshl_b32 s0, s3, 8
	s_lshl_b32 s2, s3, 7
	v_and_or_b32 v16, v8, -16, v33
	v_lshlrev_b64 v[4:5], 12, v[4:5]
	s_add_u32 s2, s12, s2
	v_ashrrev_i32_e32 v15, 31, v14
	v_lshl_add_u64 v[4:5], s[6:7], 0, v[4:5]
	v_ashrrev_i32_e32 v7, 31, v6
	s_addc_u32 s3, s13, 0
	v_lshlrev_b64 v[102:103], 11, v[14:15]
	v_ashrrev_i32_e32 v99, 31, v98
	v_ashrrev_i32_e32 v17, 31, v16
	v_lshl_add_u64 v[8:9], v[4:5], 0, s[0:1]
	v_lshlrev_b64 v[38:39], 2, v[6:7]
	v_lshl_add_u64 v[14:15], s[2:3], 0, v[102:103]
	v_lshlrev_b64 v[22:23], 1, v[98:99]
	v_lshlrev_b64 v[104:105], 11, v[16:17]
	v_ashrrev_i32_e32 v101, 31, v100
	v_lshl_add_u64 v[18:19], v[8:9], 0, v[38:39]
	v_lshl_add_u64 v[24:25], v[14:15], 0, v[22:23]
	v_lshl_add_u64 v[14:15], s[2:3], 0, v[104:105]
	v_lshlrev_b64 v[26:27], 1, v[100:101]
	global_load_dwordx4 v[6:9], v[18:19], off offset:16
	global_load_dwordx4 v[10:13], v[18:19], off
	v_lshl_add_u64 v[28:29], v[14:15], 0, v[26:27]
	global_load_dwordx4 v[14:17], v[24:25], off
	global_load_dwordx4 v[18:21], v[28:29], off
	v_lshlrev_b32_e32 v24, 10, v30
	v_or_b32_e32 v125, v24, v32
	v_xad_u32 v24, s15, 8, v2
	v_and_or_b32 v24, v24, s20, v31
	v_lshlrev_b32_e32 v25, 10, v24
	v_or_b32_e32 v122, v25, v32
	v_bfe_i32 v25, v24, 0, 22
	v_bfe_u32 v24, v24, 21, 1
	v_add_u32_e32 v28, v25, v24
	v_lshlrev_b32_e32 v24, 3, v28
	v_and_b32_e32 v28, 0x7fffffe, v28
	v_sub_u32_e32 v25, v25, v28
	v_lshl_or_b32 v28, v25, 5, v34
	v_lshlrev_b32_e32 v25, 10, v35
	v_or_b32_e32 v126, v25, v32
	v_lshlrev_b32_e32 v25, 10, v36
	v_or_b32_e32 v127, v25, v32
	v_xad_u32 v25, s17, 16, v2
	v_and_or_b32 v25, v25, s20, v31
	v_lshlrev_b32_e32 v29, 10, v25
	v_or_b32_e32 v123, v29, v32
	v_bfe_i32 v29, v25, 0, 22
	v_bfe_u32 v25, v25, 21, 1
	v_add_u32_e32 v25, v29, v25
	v_and_b32_e32 v121, 3, v2
	v_lshlrev_b32_e32 v30, 3, v25
	v_and_b32_e32 v25, 0x7fffffe, v25
	v_xad_u32 v2, s17, 24, v2
	v_sub_u32_e32 v25, v29, v25
	v_and_or_b32 v2, v2, s20, v31
	v_lshl_or_b32 v106, v25, 5, v34
	v_lshlrev_b32_e32 v25, 10, v2
	v_or_b32_e32 v124, v25, v32
	v_bfe_i32 v25, v2, 0, 22
	v_bfe_u32 v2, v2, 21, 1
	v_add_u32_e32 v2, v25, v2
	v_lshlrev_b32_e32 v29, 3, v2
	v_and_b32_e32 v2, 0x7fffffe, v2
	v_and_b32_e32 v118, 15, v0
	v_sub_u32_e32 v2, v25, v2
	v_lshlrev_b32_e32 v25, 2, v0
	v_ashrrev_i32_e32 v120, 8, v0
	v_and_or_b32 v32, v29, -16, v33
	v_lshl_or_b32 v108, v2, 5, v34
	v_and_b32_e32 v2, 48, v0
	v_and_b32_e32 v25, 32, v25
	v_lshlrev_b32_e32 v29, 6, v118
	v_and_b32_e32 v119, 63, v0
	v_and_or_b32 v24, v24, -16, v33
	v_and_or_b32 v30, v30, -16, v33
	v_lshlrev_b32_e32 v68, 13, v120
	v_bitop3_b32 v2, v29, v25, v2 bitop3:0x36
	v_ashrrev_i32_e32 v25, 31, v24
	v_lshlrev_b64 v[24:25], 12, v[24:25]
	v_lshl_add_u64 v[56:57], s[6:7], 0, v[24:25]
	v_ashrrev_i32_e32 v29, 31, v28
	v_lshl_add_u64 v[24:25], v[56:57], 0, s[0:1]
	v_lshlrev_b64 v[58:59], 2, v[28:29]
	v_ashrrev_i32_e32 v31, 31, v30
	v_lshl_add_u64 v[24:25], v[24:25], 0, v[58:59]
	v_lshlrev_b64 v[110:111], 11, v[30:31]
	v_ashrrev_i32_e32 v107, 31, v106
	v_ashrrev_i32_e32 v33, 31, v32
	global_load_dwordx4 v[40:43], v[24:25], off offset:16
	global_load_dwordx4 v[44:47], v[24:25], off
	v_lshl_add_u64 v[24:25], s[2:3], 0, v[110:111]
	v_lshlrev_b64 v[60:61], 1, v[106:107]
	v_lshlrev_b64 v[112:113], 11, v[32:33]
	v_ashrrev_i32_e32 v109, 31, v108
	v_lshl_add_u64 v[24:25], v[24:25], 0, v[60:61]
	v_lshl_add_u64 v[28:29], s[2:3], 0, v[112:113]
	v_lshlrev_b64 v[62:63], 1, v[108:109]
	v_lshl_add_u64 v[28:29], v[28:29], 0, v[62:63]
	global_load_dwordx4 v[48:51], v[24:25], off
	global_load_dwordx4 v[52:55], v[28:29], off
	s_add_i32 s0, s14, 64
	s_and_b32 s2, s0, 0x3c0
	s_lshl_b32 s0, s2, 2
	s_lshl_b32 s2, s2, 1
	v_lshl_add_u64 v[24:25], v[4:5], 0, s[0:1]
	s_add_u32 s2, s12, s2
	v_lshl_add_u64 v[24:25], v[24:25], 0, v[38:39]
	s_addc_u32 s3, s13, 0
	global_load_dwordx4 v[30:33], v[24:25], off offset:16
	global_load_dwordx4 v[34:37], v[24:25], off
	v_lshl_add_u64 v[24:25], s[2:3], 0, v[102:103]
	v_lshl_add_u64 v[64:65], v[24:25], 0, v[22:23]
	v_lshl_add_u64 v[22:23], s[2:3], 0, v[104:105]
	v_lshl_add_u64 v[66:67], v[22:23], 0, v[26:27]
	global_load_dwordx4 v[26:29], v[64:65], off
	global_load_dwordx4 v[22:25], v[66:67], off
	v_add_u32_e32 v64, 0, v125
	s_waitcnt vmcnt(10)
	v_cvt_pk_bf16_f32 v10, v10, v11
	v_cvt_pk_bf16_f32 v11, v12, v13
	v_cvt_pk_bf16_f32 v12, v6, v7
	v_add_u32_e32 v6, 0, v126
	v_cvt_pk_bf16_f32 v13, v8, v9
	ds_write_b128 v64, v[10:13]
	s_waitcnt vmcnt(9)
	ds_write_b128 v6, v[14:17] offset:32768
	v_add_u32_e32 v6, 0, v127
	s_waitcnt vmcnt(8)
	ds_write_b128 v6, v[18:21] offset:32768
	v_add_u32_e32 v10, 0, v122
	s_waitcnt vmcnt(6)
	v_cvt_pk_bf16_f32 v6, v44, v45
	v_cvt_pk_bf16_f32 v7, v46, v47
	v_cvt_pk_bf16_f32 v8, v40, v41
	v_cvt_pk_bf16_f32 v9, v42, v43
	ds_write_b128 v10, v[6:9]
	v_add_u32_e32 v6, 0, v123
	s_waitcnt vmcnt(5)
	ds_write_b128 v6, v[48:51] offset:32768
	v_add_u32_e32 v6, 0, v124
	s_waitcnt vmcnt(4)
	ds_write_b128 v6, v[52:55] offset:32768
	v_lshl_add_u64 v[6:7], v[56:57], 0, s[0:1]
	v_lshl_add_u64 v[14:15], v[6:7], 0, v[58:59]
	global_load_dwordx4 v[6:9], v[14:15], off offset:16
	global_load_dwordx4 v[10:13], v[14:15], off
	v_lshl_add_u64 v[14:15], s[2:3], 0, v[110:111]
	v_lshl_add_u64 v[40:41], v[14:15], 0, v[60:61]
	v_lshl_add_u64 v[14:15], s[2:3], 0, v[112:113]
	v_lshl_add_u64 v[42:43], v[14:15], 0, v[62:63]
	global_load_dwordx4 v[18:21], v[40:41], off
	global_load_dwordx4 v[14:17], v[42:43], off
	v_lshlrev_b32_e32 v40, 13, v121
	s_cmp_lg_u32 0, -1
	s_waitcnt lgkmcnt(0)
	s_cselect_b32 s0, 0, 0
	v_add3_u32 v128, v68, s0, v2
	s_add_i32 s0, s0, 0x8000
	v_add3_u32 v129, v40, s0, v2
	v_lshl_add_u64 v[114:115], v[4:5], 0, v[38:39]
	v_lshl_add_u64 v[116:117], v[56:57], 0, v[58:59]
	s_add_i32 s2, s14, 0x80
	s_mov_b32 s3, 0
	v_mov_b32_e32 v2, v3
	v_mov_b32_e32 v4, v3
	v_mov_b32_e32 v5, v3
	v_mov_b32_e32 v38, v3
	v_mov_b32_e32 v39, v3
	v_mov_b32_e32 v40, v3
	v_mov_b32_e32 v41, v3
	v_mov_b32_e32 v42, v3
	v_mov_b32_e32 v43, v3
	v_mov_b32_e32 v44, v3
	v_mov_b32_e32 v45, v3
	v_mov_b32_e32 v46, v3
	v_mov_b32_e32 v47, v3
	v_mov_b32_e32 v48, v3
	v_mov_b32_e32 v49, v3
	v_mov_b32_e32 v50, v3
	v_mov_b32_e32 v51, v3
	v_mov_b32_e32 v52, v3
	v_mov_b32_e32 v53, v3
	v_mov_b32_e32 v54, v3
	v_mov_b32_e32 v55, v3
	v_mov_b32_e32 v56, v3
	v_mov_b32_e32 v57, v3
	v_mov_b32_e32 v58, v3
	v_mov_b32_e32 v59, v3
	v_mov_b32_e32 v60, v3
	v_mov_b32_e32 v61, v3
	v_mov_b32_e32 v62, v3
	v_mov_b32_e32 v63, v3
	v_mov_b32_e32 v64, v3
	v_mov_b32_e32 v65, v3
	v_mov_b32_e32 v66, v3
	v_mov_b32_e32 v67, v3
	v_mov_b32_e32 v68, v3
	v_mov_b32_e32 v69, v3
	v_mov_b32_e32 v70, v3
	v_mov_b32_e32 v71, v3
	v_mov_b32_e32 v72, v3
	v_mov_b32_e32 v73, v3
	v_mov_b32_e32 v74, v3
	v_mov_b32_e32 v75, v3
	v_mov_b32_e32 v76, v3
	v_mov_b32_e32 v77, v3
	v_mov_b32_e32 v78, v3
	v_mov_b32_e32 v79, v3
	v_mov_b32_e32 v80, v3
	v_mov_b32_e32 v81, v3
	v_mov_b32_e32 v82, v3
	v_mov_b32_e32 v83, v3
	v_mov_b32_e32 v84, v3
	v_mov_b32_e32 v85, v3
	v_mov_b32_e32 v86, v3
	v_mov_b32_e32 v87, v3
	v_mov_b32_e32 v88, v3
	v_mov_b32_e32 v89, v3
	v_mov_b32_e32 v90, v3
	v_mov_b32_e32 v91, v3
	v_mov_b32_e32 v92, v3
	v_mov_b32_e32 v93, v3
	v_mov_b32_e32 v94, v3
	v_mov_b32_e32 v95, v3
	v_mov_b32_e32 v96, v3
	v_mov_b32_e32 v97, v3
	s_barrier
.LBB1_3:
	s_and_b32 s0, s3, 0x10000
	v_add_u32_e32 v158, s0, v128
	v_add_u32_e32 v159, s0, v129
	ds_read_b128 v[130:133], v159 offset:0
	ds_read_b128 v[134:137], v159 offset:0x800
	ds_read_b128 v[138:141], v159 offset:0x1000
	ds_read_b128 v[142:145], v159 offset:0x1800
	ds_read_b128 v[146:149], v158 offset:0
	ds_read_b128 v[150:153], v158 offset:0x800
	ds_read_b128 v[154:157], v158 offset:0x1000
	s_waitcnt lgkmcnt(2)
	v_mfma_f32_16x16x32_bf16 v[94:97], v[130:133], v[146:149], v[94:97]
	v_mfma_f32_16x16x32_bf16 v[90:93], v[134:137], v[146:149], v[90:93]
	v_mfma_f32_16x16x32_bf16 v[86:89], v[138:141], v[146:149], v[86:89]
	v_mfma_f32_16x16x32_bf16 v[82:85], v[142:145], v[146:149], v[82:85]
	ds_read_b128 v[146:149], v158 offset:0x1800
	s_waitcnt lgkmcnt(2)
	v_mfma_f32_16x16x32_bf16 v[78:81], v[130:133], v[150:153], v[78:81]
	v_mfma_f32_16x16x32_bf16 v[74:77], v[134:137], v[150:153], v[74:77]
	v_mfma_f32_16x16x32_bf16 v[70:73], v[138:141], v[150:153], v[70:73]
	v_mfma_f32_16x16x32_bf16 v[66:69], v[142:145], v[150:153], v[66:69]
	s_waitcnt lgkmcnt(1)
	v_mfma_f32_16x16x32_bf16 v[62:65], v[130:133], v[154:157], v[62:65]
	v_mfma_f32_16x16x32_bf16 v[58:61], v[134:137], v[154:157], v[58:61]
	v_mfma_f32_16x16x32_bf16 v[54:57], v[138:141], v[154:157], v[54:57]
	v_mfma_f32_16x16x32_bf16 v[50:53], v[142:145], v[154:157], v[50:53]
	s_waitcnt lgkmcnt(0)
	v_mfma_f32_16x16x32_bf16 v[46:49], v[130:133], v[146:149], v[46:49]
	v_mfma_f32_16x16x32_bf16 v[42:45], v[134:137], v[146:149], v[42:45]
	v_mfma_f32_16x16x32_bf16 v[38:41], v[138:141], v[146:149], v[38:41]
	v_mfma_f32_16x16x32_bf16 v[2:5], v[142:145], v[146:149], v[2:5]
	s_xor_b32 s0, s0, 0x10000
	s_and_b32 s6, s2, 0x3c0
	s_add_i32 s14, s0, 0
	s_lshl_b32 s0, s6, 2
	s_lshl_b32 s6, s6, 1
	s_add_u32 s6, s12, s6
	s_waitcnt vmcnt(6)
	v_cvt_pk_bf16_f32 v34, v34, v35
	v_cvt_pk_bf16_f32 v35, v36, v37
	v_cvt_pk_bf16_f32 v36, v30, v31
	v_cvt_pk_bf16_f32 v37, v32, v33
	v_add_u32_e32 v30, s14, v125
	s_addc_u32 s7, s13, 0
	v_add_u32_e32 v31, s14, v126
	v_add_u32_e32 v32, s14, v127
	ds_write_b128 v30, v[34:37]
	s_waitcnt vmcnt(5)
	ds_write_b128 v31, v[26:29] offset:32768
	s_waitcnt vmcnt(4)
	ds_write_b128 v32, v[22:25] offset:32768
	v_lshl_add_u64 v[22:23], s[6:7], 0, v[102:103]
	v_lshl_add_u64 v[24:25], s[6:7], 0, v[104:105]
	v_lshl_add_u64 v[130:131], v[114:115], 0, s[0:1]
	v_lshl_add_u64 v[22:23], v[98:99], 1, v[22:23]
	v_lshl_add_u64 v[24:25], v[100:101], 1, v[24:25]
	global_load_dwordx4 v[30:33], v[130:131], off offset:16
	global_load_dwordx4 v[34:37], v[130:131], off
	global_load_dwordx4 v[26:29], v[22:23], off
	s_nop 0
	global_load_dwordx4 v[22:25], v[24:25], off
	ds_read_b128 v[130:133], v159 offset:0x400
	ds_read_b128 v[134:137], v159 offset:0xc00
	ds_read_b128 v[138:141], v159 offset:0x1400
	ds_read_b128 v[142:145], v159 offset:0x1c00
	ds_read_b128 v[146:149], v158 offset:0x400
	ds_read_b128 v[150:153], v158 offset:0xc00
	ds_read_b128 v[154:157], v158 offset:0x1400
	s_waitcnt lgkmcnt(2)
	v_mfma_f32_16x16x32_bf16 v[94:97], v[130:133], v[146:149], v[94:97]
	v_mfma_f32_16x16x32_bf16 v[90:93], v[134:137], v[146:149], v[90:93]
	v_mfma_f32_16x16x32_bf16 v[86:89], v[138:141], v[146:149], v[86:89]
	v_mfma_f32_16x16x32_bf16 v[82:85], v[142:145], v[146:149], v[82:85]
	ds_read_b128 v[146:149], v158 offset:0x1c00
	s_waitcnt lgkmcnt(2)
	v_mfma_f32_16x16x32_bf16 v[78:81], v[130:133], v[150:153], v[78:81]
	v_mfma_f32_16x16x32_bf16 v[74:77], v[134:137], v[150:153], v[74:77]
	v_mfma_f32_16x16x32_bf16 v[70:73], v[138:141], v[150:153], v[70:73]
	v_mfma_f32_16x16x32_bf16 v[66:69], v[142:145], v[150:153], v[66:69]
	s_waitcnt lgkmcnt(1)
	v_mfma_f32_16x16x32_bf16 v[62:65], v[130:133], v[154:157], v[62:65]
	v_mfma_f32_16x16x32_bf16 v[58:61], v[134:137], v[154:157], v[58:61]
	v_mfma_f32_16x16x32_bf16 v[54:57], v[138:141], v[154:157], v[54:57]
	v_mfma_f32_16x16x32_bf16 v[50:53], v[142:145], v[154:157], v[50:53]
	s_waitcnt lgkmcnt(0)
	v_mfma_f32_16x16x32_bf16 v[46:49], v[130:133], v[146:149], v[46:49]
	v_mfma_f32_16x16x32_bf16 v[42:45], v[134:137], v[146:149], v[42:45]
	v_mfma_f32_16x16x32_bf16 v[38:41], v[138:141], v[146:149], v[38:41]
	v_mfma_f32_16x16x32_bf16 v[2:5], v[142:145], v[146:149], v[2:5]
	v_add_u32_e32 v130, s14, v122
	s_waitcnt vmcnt(6)
	v_cvt_pk_bf16_f32 v10, v10, v11
	v_cvt_pk_bf16_f32 v11, v12, v13
	v_cvt_pk_bf16_f32 v12, v6, v7
	v_add_u32_e32 v6, s14, v123
	v_cvt_pk_bf16_f32 v13, v8, v9
	ds_write_b128 v130, v[10:13]
	s_waitcnt vmcnt(5)
	ds_write_b128 v6, v[18:21] offset:32768
	v_add_u32_e32 v6, s14, v124
	s_waitcnt vmcnt(4)
	ds_write_b128 v6, v[14:17] offset:32768
	v_lshl_add_u64 v[14:15], s[6:7], 0, v[110:111]
	v_lshl_add_u64 v[16:17], s[6:7], 0, v[112:113]
	v_lshl_add_u64 v[10:11], v[116:117], 0, s[0:1]
	v_lshl_add_u64 v[14:15], v[106:107], 1, v[14:15]
	v_lshl_add_u64 v[16:17], v[108:109], 1, v[16:17]
	global_load_dwordx4 v[6:9], v[10:11], off offset:16
	s_nop 0
	global_load_dwordx4 v[10:13], v[10:11], off
	s_nop 0
	global_load_dwordx4 v[18:21], v[14:15], off
	s_nop 0
	global_load_dwordx4 v[14:17], v[16:17], off
	s_waitcnt lgkmcnt(0)
	s_add_i32 s2, s2, 64
	s_add_i32 s3, s3, 0x10000
	s_cmp_lg_u32 s3, 0xe0000
	s_barrier
	s_cbranch_scc1 .LBB1_3
	ds_read_b128 v[98:101], v129 offset:0
	ds_read_b128 v[102:105], v129 offset:0x800
	ds_read_b128 v[106:109], v129 offset:0x1000
	ds_read_b128 v[110:113], v129 offset:0x1800
	ds_read_b128 v[114:117], v128 offset:0
	ds_read_b128 v[130:133], v128 offset:0x800
	ds_read_b128 v[134:137], v128 offset:0x1000
	s_nop 0
	s_waitcnt lgkmcnt(2)
	s_nop 0
	v_mfma_f32_16x16x32_bf16 v[94:97], v[98:101], v[114:117], v[94:97]
	v_mfma_f32_16x16x32_bf16 v[90:93], v[102:105], v[114:117], v[90:93]
	v_mfma_f32_16x16x32_bf16 v[86:89], v[106:109], v[114:117], v[86:89]
	v_mfma_f32_16x16x32_bf16 v[82:85], v[110:113], v[114:117], v[82:85]
	ds_read_b128 v[114:117], v128 offset:0x1800
	s_waitcnt lgkmcnt(2)
	s_nop 0
	v_mfma_f32_16x16x32_bf16 v[78:81], v[98:101], v[130:133], v[78:81]
	v_mfma_f32_16x16x32_bf16 v[74:77], v[102:105], v[130:133], v[74:77]
	v_mfma_f32_16x16x32_bf16 v[70:73], v[106:109], v[130:133], v[70:73]
	v_mfma_f32_16x16x32_bf16 v[66:69], v[110:113], v[130:133], v[66:69]
	s_waitcnt lgkmcnt(1)
	s_nop 0
	v_mfma_f32_16x16x32_bf16 v[62:65], v[98:101], v[134:137], v[62:65]
	v_mfma_f32_16x16x32_bf16 v[58:61], v[102:105], v[134:137], v[58:61]
	v_mfma_f32_16x16x32_bf16 v[54:57], v[106:109], v[134:137], v[54:57]
	v_mfma_f32_16x16x32_bf16 v[50:53], v[110:113], v[134:137], v[50:53]
	s_waitcnt lgkmcnt(0)
	s_nop 0
	v_mfma_f32_16x16x32_bf16 v[46:49], v[98:101], v[114:117], v[46:49]
	v_mfma_f32_16x16x32_bf16 v[42:45], v[102:105], v[114:117], v[42:45]
	v_mfma_f32_16x16x32_bf16 v[38:41], v[106:109], v[114:117], v[38:41]
	v_mfma_f32_16x16x32_bf16 v[2:5], v[110:113], v[114:117], v[2:5]
	v_add_u32_e32 v98, s18, v125
	s_waitcnt vmcnt(6)
	v_cvt_pk_bf16_f32 v34, v34, v35
	v_cvt_pk_bf16_f32 v35, v36, v37
	v_cvt_pk_bf16_f32 v36, v30, v31
	v_add_u32_e32 v30, s19, v126
	v_cvt_pk_bf16_f32 v37, v32, v33
	ds_write_b128 v98, v[34:37]
	s_waitcnt vmcnt(5)
	ds_write_b128 v30, v[26:29]
	v_add_u32_e32 v26, s19, v127
	s_waitcnt vmcnt(4)
	ds_write_b128 v26, v[22:25]
	ds_read_b128 v[22:25], v129 offset:0x400
	ds_read_b128 v[26:29], v129 offset:0xc00
	ds_read_b128 v[30:33], v129 offset:0x1400
	ds_read_b128 v[34:37], v129 offset:0x1c00
	ds_read_b128 v[98:101], v128 offset:0x400
	ds_read_b128 v[102:105], v128 offset:0xc00
	ds_read_b128 v[106:109], v128 offset:0x1400
	s_nop 0
	s_waitcnt lgkmcnt(2)
	s_nop 0
	v_mfma_f32_16x16x32_bf16 v[94:97], v[22:25], v[98:101], v[94:97]
	v_mfma_f32_16x16x32_bf16 v[90:93], v[26:29], v[98:101], v[90:93]
	v_mfma_f32_16x16x32_bf16 v[86:89], v[30:33], v[98:101], v[86:89]
	v_mfma_f32_16x16x32_bf16 v[82:85], v[34:37], v[98:101], v[82:85]
	ds_read_b128 v[98:101], v128 offset:0x1c00
	s_waitcnt lgkmcnt(2)
	s_nop 0
	v_mfma_f32_16x16x32_bf16 v[78:81], v[22:25], v[102:105], v[78:81]
	v_mfma_f32_16x16x32_bf16 v[74:77], v[26:29], v[102:105], v[74:77]
	v_mfma_f32_16x16x32_bf16 v[70:73], v[30:33], v[102:105], v[70:73]
	v_mfma_f32_16x16x32_bf16 v[66:69], v[34:37], v[102:105], v[66:69]
	s_waitcnt lgkmcnt(1)
	s_nop 0
	v_mfma_f32_16x16x32_bf16 v[62:65], v[22:25], v[106:109], v[62:65]
	v_mfma_f32_16x16x32_bf16 v[58:61], v[26:29], v[106:109], v[58:61]
	v_mfma_f32_16x16x32_bf16 v[54:57], v[30:33], v[106:109], v[54:57]
	v_mfma_f32_16x16x32_bf16 v[50:53], v[34:37], v[106:109], v[50:53]
	s_waitcnt lgkmcnt(0)
	s_nop 0
	v_mfma_f32_16x16x32_bf16 v[22:25], v[22:25], v[98:101], v[46:49]
	v_mfma_f32_16x16x32_bf16 v[26:29], v[26:29], v[98:101], v[42:45]
	v_mfma_f32_16x16x32_bf16 v[30:33], v[30:33], v[98:101], v[38:41]
	v_mfma_f32_16x16x32_bf16 v[2:5], v[34:37], v[98:101], v[2:5]
	v_add_u32_e32 v34, s18, v122
	s_waitcnt vmcnt(2)
	v_cvt_pk_bf16_f32 v10, v10, v11
	v_cvt_pk_bf16_f32 v11, v12, v13
	v_cvt_pk_bf16_f32 v12, v6, v7
	v_add_u32_e32 v6, s19, v123
	s_lshl_b64 s[0:1], s[4:5], 1
	v_cvt_pk_bf16_f32 v13, v8, v9
	ds_write_b128 v34, v[10:13]
	s_waitcnt vmcnt(1)
	ds_write_b128 v6, v[18:21]
	v_add_u32_e32 v6, s19, v124
	s_add_u32 s0, s10, s0
	s_waitcnt vmcnt(0)
	ds_write_b128 v6, v[14:17]
	s_addc_u32 s1, s11, s1
	s_lshl_b32 s2, s16, 9
	s_waitcnt lgkmcnt(0)
	s_barrier
	v_add_u32_e32 v110, 0x10000, v128
	v_add_u32_e32 v102, 0x10000, v129
	ds_read_b128 v[6:9], v102 offset:0
	ds_read_b128 v[10:13], v102 offset:0x800
	ds_read_b128 v[14:17], v102 offset:0x1000
	ds_read_b128 v[18:21], v102 offset:0x1800
	ds_read_b128 v[34:37], v110 offset:0
	ds_read_b128 v[38:41], v110 offset:0x800
	ds_read_b128 v[42:45], v110 offset:0x1000
	s_add_u32 s0, s0, s2
	s_addc_u32 s1, s1, 0
	s_lshl_b32 s2, s16, 10
	s_waitcnt lgkmcnt(2)
	s_add_u32 s2, s8, s2
	v_mfma_f32_16x16x32_bf16 v[46:49], v[6:9], v[34:37], v[94:97]
	s_addc_u32 s3, s9, 0
	v_mfma_f32_16x16x32_bf16 v[90:93], v[10:13], v[34:37], v[90:93]
	v_mfma_f32_16x16x32_bf16 v[86:89], v[14:17], v[34:37], v[86:89]
	v_mfma_f32_16x16x32_bf16 v[34:37], v[18:21], v[34:37], v[82:85]
	ds_read_b128 v[82:85], v110 offset:0x1800
	s_waitcnt lgkmcnt(2)
	s_nop 0
	v_mfma_f32_16x16x32_bf16 v[78:81], v[6:9], v[38:41], v[78:81]
	v_mfma_f32_16x16x32_bf16 v[74:77], v[10:13], v[38:41], v[74:77]
	v_mfma_f32_16x16x32_bf16 v[70:73], v[14:17], v[38:41], v[70:73]
	v_mfma_f32_16x16x32_bf16 v[38:41], v[18:21], v[38:41], v[66:69]
	s_waitcnt lgkmcnt(1)
	s_nop 0
	v_mfma_f32_16x16x32_bf16 v[62:65], v[6:9], v[42:45], v[62:65]
	v_mfma_f32_16x16x32_bf16 v[58:61], v[10:13], v[42:45], v[58:61]
	v_mfma_f32_16x16x32_bf16 v[54:57], v[14:17], v[42:45], v[54:57]
	v_mfma_f32_16x16x32_bf16 v[42:45], v[18:21], v[42:45], v[50:53]
	s_waitcnt lgkmcnt(0)
	s_nop 0
	v_mfma_f32_16x16x32_bf16 v[50:53], v[6:9], v[82:85], v[22:25]
	v_mfma_f32_16x16x32_bf16 v[66:69], v[10:13], v[82:85], v[26:29]
	v_mfma_f32_16x16x32_bf16 v[94:97], v[14:17], v[82:85], v[30:33]
	v_mfma_f32_16x16x32_bf16 v[2:5], v[18:21], v[82:85], v[2:5]
	ds_read_b128 v[18:21], v102 offset:0x400
	ds_read_b128 v[82:85], v102 offset:0xc00
	ds_read_b128 v[98:101], v102 offset:0x1400
	ds_read_b128 v[102:105], v102 offset:0x1c00
	ds_read_b128 v[6:9], v110 offset:0x400
	ds_read_b128 v[10:13], v110 offset:0xc00
	ds_read_b128 v[106:109], v110 offset:0x1400
	s_nop 0
	s_waitcnt lgkmcnt(2)
	s_nop 0
	v_mfma_f32_16x16x32_bf16 v[46:49], v[18:21], v[6:9], v[46:49]
	v_mfma_f32_16x16x32_bf16 v[90:93], v[82:85], v[6:9], v[90:93]
	v_mfma_f32_16x16x32_bf16 v[30:33], v[98:101], v[6:9], v[86:89]
	v_mfma_f32_16x16x32_bf16 v[14:17], v[102:105], v[6:9], v[34:37]
	ds_read_b128 v[86:89], v110 offset:0x1c00
	s_waitcnt lgkmcnt(2)
	s_nop 0
	v_mfma_f32_16x16x32_bf16 v[78:81], v[18:21], v[10:13], v[78:81]
	v_mfma_f32_16x16x32_bf16 v[74:77], v[82:85], v[10:13], v[74:77]
	v_mfma_f32_16x16x32_bf16 v[26:29], v[98:101], v[10:13], v[70:73]
	v_mfma_f32_16x16x32_bf16 v[10:13], v[102:105], v[10:13], v[38:41]
	s_waitcnt lgkmcnt(1)
	s_nop 0
	v_mfma_f32_16x16x32_bf16 v[62:65], v[18:21], v[106:109], v[62:65]
	v_mfma_f32_16x16x32_bf16 v[38:41], v[82:85], v[106:109], v[58:61]
	v_mfma_f32_16x16x32_bf16 v[22:25], v[98:101], v[106:109], v[54:57]
	v_mfma_f32_16x16x32_bf16 v[6:9], v[102:105], v[106:109], v[42:45]
	s_waitcnt lgkmcnt(0)
	s_nop 0
	v_mfma_f32_16x16x32_bf16 v[42:45], v[18:21], v[86:89], v[50:53]
	v_mfma_f32_16x16x32_bf16 v[34:37], v[82:85], v[86:89], v[66:69]
	v_mfma_f32_16x16x32_bf16 v[18:21], v[98:101], v[86:89], v[94:97]
	v_mfma_f32_16x16x32_bf16 v[2:5], v[102:105], v[86:89], v[2:5]
	v_lshrrev_b32_e32 v50, 2, v119
	v_and_b32_e32 v50, 12, v50
	v_lshl_or_b32 v66, v121, 6, v50
	v_lshlrev_b32_e32 v67, 2, v66
	s_waitcnt lgkmcnt(0)
	s_barrier
	global_load_dwordx4 v[50:53], v67, s[2:3]
	global_load_dwordx4 v[54:57], v67, s[2:3] offset:64
	v_lshrrev_b32_e32 v58, 1, v119
	v_lshl_or_b32 v59, v120, 6, v118
	v_and_b32_e32 v68, 8, v58
	v_lshl_add_u32 v69, v59, 9, 0
	v_or_b32_e32 v70, 16, v59
	v_or_b32_e32 v71, 48, v59
	v_lshrrev_b32_e32 v58, 3, v66
	v_or_b32_e32 v59, 16, v66
	v_bitop3_b32 v83, v70, v58, 31 bitop3:0x6c
	v_lshrrev_b32_e32 v85, 3, v59
	v_lshl_add_u32 v72, v70, 9, 0
	v_xor_b32_e32 v82, v58, v118
	v_bitop3_b32 v84, v71, v58, 31 bitop3:0x6c
	v_lshlrev_b32_e32 v83, 4, v83
	v_xor_b32_e32 v86, v85, v118
	v_lshl_add_u32 v73, v71, 9, 0
	v_lshlrev_b32_e32 v82, 4, v82
	v_lshlrev_b32_e32 v84, 4, v84
	v_add3_u32 v83, v72, v83, v68
	v_lshlrev_b32_e32 v86, 4, v86
	global_load_dwordx4 v[58:61], v67, s[2:3] offset:128
	v_add3_u32 v82, v69, v82, v68
	v_add3_u32 v84, v73, v84, v68
	v_add3_u32 v86, v69, v86, v68
	s_waitcnt vmcnt(2)
	v_add_f32_e32 v46, v46, v50
	v_add_f32_e32 v47, v47, v51
	v_add_f32_e32 v48, v48, v52
	v_add_f32_e32 v49, v49, v53
	v_add_f32_e32 v78, v78, v50
	v_add_f32_e32 v79, v79, v51
	v_add_f32_e32 v80, v80, v52
	v_add_f32_e32 v81, v81, v53
	v_add_f32_e32 v62, v62, v50
	v_add_f32_e32 v63, v63, v51
	v_add_f32_e32 v42, v42, v50
	v_add_f32_e32 v43, v43, v51
	v_add_f32_e32 v44, v44, v52
	v_add_f32_e32 v45, v45, v53
	s_waitcnt vmcnt(1)
	v_add_f32_e32 v50, v90, v54
	v_add_f32_e32 v51, v91, v55
	v_add_f32_e32 v64, v64, v52
	v_add_f32_e32 v65, v65, v53
	v_add_f32_e32 v52, v92, v56
	v_add_f32_e32 v53, v93, v57
	v_max_f32_e32 v46, 0, v46
	v_max_f32_e32 v47, 0, v47
	v_max_f32_e32 v48, 0, v48
	v_max_f32_e32 v49, 0, v49
	v_max_f32_e32 v78, 0, v78
	v_max_f32_e32 v79, 0, v79
	v_max_f32_e32 v80, 0, v80
	v_max_f32_e32 v81, 0, v81
	v_max_f32_e32 v88, 0, v43
	v_max_f32_e32 v89, 0, v44
	v_max_f32_e32 v90, 0, v45
	v_max_f32_e32 v50, 0, v50
	v_max_f32_e32 v51, 0, v51
	v_cvt_pk_bf16_f32 v43, v48, v49
	v_cvt_pk_bf16_f32 v44, v78, v79
	v_cvt_pk_bf16_f32 v45, v80, v81
	v_max_f32_e32 v62, 0, v62
	v_max_f32_e32 v63, 0, v63
	v_max_f32_e32 v64, 0, v64
	v_max_f32_e32 v65, 0, v65
	v_max_f32_e32 v87, 0, v42
	v_max_f32_e32 v52, 0, v52
	v_max_f32_e32 v53, 0, v53
	v_cvt_pk_bf16_f32 v42, v46, v47
	v_cvt_pk_bf16_f32 v46, v62, v63
	v_cvt_pk_bf16_f32 v47, v64, v65
	v_cvt_pk_bf16_f32 v48, v87, v88
	v_cvt_pk_bf16_f32 v49, v89, v90
	v_cvt_pk_bf16_f32 v50, v50, v51
	v_cvt_pk_bf16_f32 v51, v52, v53
	ds_write_b64 v83, v[44:45]
	ds_write2st64_b64 v82, v[42:43], v[46:47] offset1:32
	ds_write_b64 v84, v[48:49]
	ds_write_b64 v86, v[50:51]
	v_add_f32_e32 v43, v76, v56
	v_add_f32_e32 v44, v77, v57
	v_max_f32_e32 v43, 0, v43
	v_max_f32_e32 v44, 0, v44
	v_add_f32_e32 v42, v75, v55
	v_cvt_pk_bf16_f32 v43, v43, v44
	v_bitop3_b32 v44, v85, v70, 31 bitop3:0x78
	v_add_f32_e32 v74, v74, v54
	v_max_f32_e32 v42, 0, v42
	v_lshlrev_b32_e32 v44, 4, v44
	v_max_f32_e32 v74, 0, v74
	v_cvt_pk_bf16_f32 v42, v74, v42
	v_add3_u32 v44, v72, v44, v68
	ds_write_b64 v44, v[42:43]
	global_load_dwordx4 v[42:45], v67, s[2:3] offset:192
	v_add_f32_e32 v34, v34, v54
	v_add_f32_e32 v35, v35, v55
	v_add_f32_e32 v36, v36, v56
	v_max_f32_e32 v34, 0, v34
	v_max_f32_e32 v35, 0, v35
	v_max_f32_e32 v36, 0, v36
	v_add_f32_e32 v37, v37, v57
	v_max_f32_e32 v37, 0, v37
	v_cvt_pk_bf16_f32 v34, v34, v35
	v_cvt_pk_bf16_f32 v35, v36, v37
	v_bitop3_b32 v36, v85, v71, 31 bitop3:0x78
	v_add_f32_e32 v38, v38, v54
	v_add_f32_e32 v39, v39, v55
	v_lshlrev_b32_e32 v36, 4, v36
	v_max_f32_e32 v38, 0, v38
	v_max_f32_e32 v39, 0, v39
	v_add_f32_e32 v40, v40, v56
	v_add_f32_e32 v41, v41, v57
	v_add3_u32 v36, v73, v36, v68
	v_max_f32_e32 v40, 0, v40
	v_max_f32_e32 v41, 0, v41
	v_cvt_pk_bf16_f32 v38, v38, v39
	v_cvt_pk_bf16_f32 v39, v40, v41
	ds_write_b64 v86, v[38:39] offset:16384
	ds_write_b64 v36, v[34:35]
	v_or_b32_e32 v34, 32, v66
	s_waitcnt vmcnt(1)
	v_add_f32_e32 v30, v30, v58
	v_add_f32_e32 v31, v31, v59
	v_add_f32_e32 v32, v32, v60
	v_add_f32_e32 v26, v26, v58
	v_add_f32_e32 v27, v27, v59
	v_add_f32_e32 v28, v28, v60
	v_add_f32_e32 v18, v18, v58
	v_add_f32_e32 v19, v19, v59
	v_add_f32_e32 v20, v20, v60
	v_lshrrev_b32_e32 v34, 3, v34
	v_max_f32_e32 v30, 0, v30
	v_max_f32_e32 v31, 0, v31
	v_max_f32_e32 v32, 0, v32
	v_add_f32_e32 v33, v33, v61
	v_max_f32_e32 v26, 0, v26
	v_max_f32_e32 v27, 0, v27
	v_max_f32_e32 v28, 0, v28
	v_add_f32_e32 v29, v29, v61
	v_max_f32_e32 v18, 0, v18
	v_max_f32_e32 v19, 0, v19
	v_max_f32_e32 v20, 0, v20
	v_add_f32_e32 v21, v21, v61
	v_max_f32_e32 v33, 0, v33
	v_cvt_pk_bf16_f32 v30, v30, v31
	v_cvt_pk_bf16_f32 v31, v32, v33
	v_xor_b32_e32 v32, v34, v118
	v_max_f32_e32 v29, 0, v29
	v_cvt_pk_bf16_f32 v26, v26, v27
	v_cvt_pk_bf16_f32 v27, v28, v29
	v_bitop3_b32 v28, v34, v70, 31 bitop3:0x78
	v_max_f32_e32 v21, 0, v21
	v_cvt_pk_bf16_f32 v18, v18, v19
	v_cvt_pk_bf16_f32 v19, v20, v21
	v_bitop3_b32 v20, v34, v71, 31 bitop3:0x78
	v_lshlrev_b32_e32 v32, 4, v32
	v_lshlrev_b32_e32 v28, 4, v28
	v_add_f32_e32 v22, v22, v58
	v_add_f32_e32 v23, v23, v59
	v_lshlrev_b32_e32 v20, 4, v20
	v_add3_u32 v32, v69, v32, v68
	v_add3_u32 v28, v72, v28, v68
	v_max_f32_e32 v22, 0, v22
	v_max_f32_e32 v23, 0, v23
	v_add_f32_e32 v24, v24, v60
	v_add_f32_e32 v25, v25, v61
	v_add3_u32 v20, v73, v20, v68
	ds_write_b64 v32, v[30:31]
	ds_write_b64 v28, v[26:27]
	v_max_f32_e32 v24, 0, v24
	v_max_f32_e32 v25, 0, v25
	v_cvt_pk_bf16_f32 v22, v22, v23
	v_cvt_pk_bf16_f32 v23, v24, v25
	ds_write_b64 v32, v[22:23] offset:16384
	ds_write_b64 v20, v[18:19]
	v_or_b32_e32 v18, 48, v66
	s_waitcnt vmcnt(0)
	v_add_f32_e32 v14, v14, v42
	v_add_f32_e32 v15, v15, v43
	v_add_f32_e32 v16, v16, v44
	v_add_f32_e32 v10, v10, v42
	v_add_f32_e32 v11, v11, v43
	v_add_f32_e32 v12, v12, v44
	v_add_f32_e32 v2, v2, v42
	v_add_f32_e32 v3, v3, v43
	v_add_f32_e32 v4, v4, v44
	v_lshrrev_b32_e32 v18, 3, v18
	v_max_f32_e32 v14, 0, v14
	v_max_f32_e32 v15, 0, v15
	v_max_f32_e32 v16, 0, v16
	v_add_f32_e32 v17, v17, v45
	v_max_f32_e32 v10, 0, v10
	v_max_f32_e32 v11, 0, v11
	v_max_f32_e32 v12, 0, v12
	v_add_f32_e32 v13, v13, v45
	v_max_f32_e32 v2, 0, v2
	v_max_f32_e32 v3, 0, v3
	v_max_f32_e32 v4, 0, v4
	v_add_f32_e32 v5, v5, v45
	v_max_f32_e32 v17, 0, v17
	v_cvt_pk_bf16_f32 v14, v14, v15
	v_cvt_pk_bf16_f32 v15, v16, v17
	v_xor_b32_e32 v16, v18, v118
	v_max_f32_e32 v13, 0, v13
	v_cvt_pk_bf16_f32 v10, v10, v11
	v_cvt_pk_bf16_f32 v11, v12, v13
	v_bitop3_b32 v12, v18, v70, 31 bitop3:0x78
	v_max_f32_e32 v5, 0, v5
	v_cvt_pk_bf16_f32 v2, v2, v3
	v_cvt_pk_bf16_f32 v3, v4, v5
	v_bitop3_b32 v4, v18, v71, 31 bitop3:0x78
	v_lshlrev_b32_e32 v16, 4, v16
	v_lshlrev_b32_e32 v12, 4, v12
	v_add_f32_e32 v6, v6, v42
	v_add_f32_e32 v7, v7, v43
	v_lshlrev_b32_e32 v4, 4, v4
	v_add3_u32 v16, v69, v16, v68
	v_add3_u32 v12, v72, v12, v68
	v_max_f32_e32 v6, 0, v6
	v_max_f32_e32 v7, 0, v7
	v_add_f32_e32 v8, v8, v44
	v_add_f32_e32 v9, v9, v45
	v_add3_u32 v4, v73, v4, v68
	ds_write_b64 v16, v[14:15]
	ds_write_b64 v12, v[10:11]
	v_max_f32_e32 v8, 0, v8
	v_max_f32_e32 v9, 0, v9
	v_cvt_pk_bf16_f32 v6, v6, v7
	v_cvt_pk_bf16_f32 v7, v8, v9
	ds_write_b64 v16, v[6:7] offset:16384
	ds_write_b64 v4, v[2:3]
	v_and_b32_e32 v2, 0x1f0, v1
	v_mov_b32_e32 v3, 0
	v_lshl_add_u64 v[2:3], s[0:1], 0, v[2:3]
	s_mov_b64 s[0:1], 0x2000000
	v_ashrrev_i32_e32 v6, 5, v0
	v_lshl_add_u64 v[10:11], v[2:3], 0, s[0:1]
	v_xor_b32_e32 v2, v6, v0
	v_lshlrev_b32_e32 v2, 4, v2
	v_lshlrev_b32_e32 v1, 9, v6
	v_and_b32_e32 v2, 0x1f0, v2
	v_add3_u32 v1, 0, v1, v2
	s_waitcnt lgkmcnt(0)
	s_barrier
	ds_read_b128 v[2:5], v1
	v_ashrrev_i32_e32 v7, 31, v6
	v_add_u32_e32 v1, 0x200, v0
	v_lshlrev_b64 v[6:7], 11, v[6:7]
	v_ashrrev_i32_e32 v14, 5, v1
	v_lshl_add_u64 v[12:13], v[10:11], 0, v[6:7]
	v_xor_b32_e32 v6, v14, v0
	v_lshlrev_b32_e32 v6, 4, v6
	v_lshlrev_b32_e32 v1, 9, v14
	v_and_b32_e32 v6, 0x1f0, v6
	v_add3_u32 v1, 0, v1, v6
	ds_read_b128 v[6:9], v1
	v_ashrrev_i32_e32 v15, 31, v14
	s_waitcnt lgkmcnt(1)
	global_store_dwordx4 v[12:13], v[2:5], off sc1
	v_add_u32_e32 v1, 0x400, v0
	s_nop 0
	v_lshlrev_b64 v[2:3], 11, v[14:15]
	v_lshl_add_u64 v[2:3], v[10:11], 0, v[2:3]
	s_waitcnt lgkmcnt(0)
	global_store_dwordx4 v[2:3], v[6:9], off sc1
	s_nop 1
	v_ashrrev_i32_e32 v6, 5, v1
	v_xor_b32_e32 v2, v6, v0
	v_lshlrev_b32_e32 v2, 4, v2
	v_lshlrev_b32_e32 v1, 9, v6
	v_and_b32_e32 v2, 0x1f0, v2
	v_add3_u32 v1, 0, v1, v2
	ds_read_b128 v[2:5], v1
	v_ashrrev_i32_e32 v7, 31, v6
	v_add_u32_e32 v1, 0x600, v0
	v_lshlrev_b64 v[6:7], 11, v[6:7]
	v_ashrrev_i32_e32 v14, 5, v1
	v_lshl_add_u64 v[12:13], v[10:11], 0, v[6:7]
	v_xor_b32_e32 v6, v14, v0
	v_lshlrev_b32_e32 v6, 4, v6
	v_lshlrev_b32_e32 v1, 9, v14
	v_and_b32_e32 v6, 0x1f0, v6
	v_add3_u32 v1, 0, v1, v6
	ds_read_b128 v[6:9], v1
	v_ashrrev_i32_e32 v15, 31, v14
	s_waitcnt lgkmcnt(1)
	global_store_dwordx4 v[12:13], v[2:5], off sc1
	v_add_u32_e32 v1, 0x800, v0
	s_nop 0
	v_lshlrev_b64 v[2:3], 11, v[14:15]
	v_lshl_add_u64 v[2:3], v[10:11], 0, v[2:3]
	s_waitcnt lgkmcnt(0)
	global_store_dwordx4 v[2:3], v[6:9], off sc1
	s_nop 1
	v_ashrrev_i32_e32 v6, 5, v1
	v_xor_b32_e32 v2, v6, v0
	v_lshlrev_b32_e32 v2, 4, v2
	v_lshlrev_b32_e32 v1, 9, v6
	v_and_b32_e32 v2, 0x1f0, v2
	v_add3_u32 v1, 0, v1, v2
	ds_read_b128 v[2:5], v1
	v_ashrrev_i32_e32 v7, 31, v6
	v_add_u32_e32 v1, 0xa00, v0
	v_lshlrev_b64 v[6:7], 11, v[6:7]
	v_ashrrev_i32_e32 v14, 5, v1
	v_lshl_add_u64 v[12:13], v[10:11], 0, v[6:7]
	v_xor_b32_e32 v6, v14, v0
	v_lshlrev_b32_e32 v6, 4, v6
	v_lshlrev_b32_e32 v1, 9, v14
	v_and_b32_e32 v6, 0x1f0, v6
	v_add3_u32 v1, 0, v1, v6
	ds_read_b128 v[6:9], v1
	v_ashrrev_i32_e32 v15, 31, v14
	s_waitcnt lgkmcnt(1)
	global_store_dwordx4 v[12:13], v[2:5], off sc1
	v_add_u32_e32 v1, 0xc00, v0
	s_nop 0
	v_lshlrev_b64 v[2:3], 11, v[14:15]
	v_lshl_add_u64 v[2:3], v[10:11], 0, v[2:3]
	s_waitcnt lgkmcnt(0)
	global_store_dwordx4 v[2:3], v[6:9], off sc1
	s_nop 1
	v_ashrrev_i32_e32 v6, 5, v1
	v_xor_b32_e32 v2, v6, v0
	v_lshlrev_b32_e32 v2, 4, v2
	v_lshlrev_b32_e32 v1, 9, v6
	v_and_b32_e32 v2, 0x1f0, v2
	v_add3_u32 v1, 0, v1, v2
	ds_read_b128 v[2:5], v1
	v_add_u32_e32 v1, 0xe00, v0
	v_ashrrev_i32_e32 v14, 5, v1
	v_xor_b32_e32 v0, v14, v0
	v_lshlrev_b32_e32 v0, 4, v0
	v_ashrrev_i32_e32 v7, 31, v6
	v_lshlrev_b32_e32 v1, 9, v14
	v_and_b32_e32 v0, 0x1f0, v0
	v_lshlrev_b64 v[6:7], 11, v[6:7]
	v_add3_u32 v0, 0, v1, v0
	v_lshl_add_u64 v[12:13], v[10:11], 0, v[6:7]
	ds_read_b128 v[6:9], v0
	v_ashrrev_i32_e32 v15, 31, v14
	v_lshlrev_b64 v[0:1], 11, v[14:15]
	v_lshl_add_u64 v[0:1], v[10:11], 0, v[0:1]
	s_waitcnt lgkmcnt(1)
	global_store_dwordx4 v[12:13], v[2:5], off sc1
	s_waitcnt lgkmcnt(0)
	global_store_dwordx4 v[0:1], v[6:9], off sc1
	s_endpgm
